# plus: P1 (input projection) epilogue output stores marked non-temporal so the streamed outputs do not evict GEMM operand tiles from L2
# speedup vs baseline: 1.0226x; 1.0226x over previous
; DI unsigned cvt_pk_bf16(float lo, float hi) { unsigned r; asm volatile("v_cvt_pk_bf16_f32 %0, %1, %2" : "=v"(r) : "v"(lo), "v"(hi)); return r; }
;     DI void operator()(const f32x4 (&acc)[2][2][4][2], const pg8::Unit& u, int wr, int wc, int fr, int fq) const {
;     ...
;                         const int row = row0 + ai * 128 + m * 16, b = row >> 11, s = row & 2047;
;                         const int pos = ((s & ((1 << sh) - 1)) << (11 - sh)) + (s >> sh);
;                         float v[8];
; #pragma unroll
;                         for (int e = 0; e < 4; ++e) { v[e] = acc[ai][bj][m][0][e]; v[4 + e] = acc[ai][bj][m][1][e]; }
;                         if (kind < 2) {
;                             const float sc = (kind == 0) ? 0.08838834764831845f : 1.0f;
;                             u32x4 w; w.x = pg8::cvt_pk_bf16(v[0] * sc, v[1] * sc); w.y = pg8::cvt_pk_bf16(v[2] * sc, v[3] * sc); w.z = pg8::cvt_pk_bf16(v[4] * sc, v[5] * sc); w.w = pg8::cvt_pk_bf16(v[6] * sc, v[7] * sc);
;                             bf16_t* base = (bf16_t*)(ws + (kind == 0 ? WS_QB : WS_KB));
;                             const size_t o = ((size_t)((b * 12 + head) * 64 + (pos >> 5)) * 8 + (cw >> 4)) * 512 + (size_t)(((pos & 31) + 32 * ((cw >> 3) & 1)) * 8);
;                             if (NOSTORE) asm volatile("" :: "v"(w)); else st16_stream(base + o, w);
.LBB0_109:
	v_and_or_b32 v5, v4, 31, v174
	v_cndmask_b32_e64 v3, 1.0, v178, s[4:5]
	s_andn2_b64 vcc, exec, s[12:13]
	v_lshlrev_b32_e32 v4, 1, v148
	v_lshlrev_b32_e32 v6, 4, v5
	s_cbranch_vccnz .LBB0_111
	v_mul_f32_e32 v5, v3, v136
	v_mul_f32_e32 v7, v3, v137
	v_cvt_pk_bf16_f32 v164, v5, v7
	v_mul_f32_e32 v5, v3, v138
	v_mul_f32_e32 v7, v3, v139
	v_cvt_pk_bf16_f32 v165, v5, v7
	v_mul_f32_e32 v5, v3, v132
	s_add_u32 s4, s18, s14
	v_ashrrev_i32_e32 v9, 31, v8
	v_mul_f32_e32 v7, v3, v133
	v_cvt_pk_bf16_f32 v166, v5, v7
	v_mul_f32_e32 v5, v3, v134
	s_addc_u32 s5, s19, 0
	v_lshlrev_b64 v[8:9], 13, v[8:9]
	v_mul_f32_e32 v7, v3, v135
	v_cvt_pk_bf16_f32 v167, v5, v7
	v_lshl_add_u64 v[8:9], s[4:5], 0, v[8:9]
	v_mov_b32_e32 v5, v2
	v_lshl_add_u64 v[8:9], v[8:9], 0, v[4:5]
	v_mov_b32_e32 v7, v2
	v_lshl_add_u64 v[8:9], v[8:9], 0, v[6:7]
	global_store_dwordx4 v[8:9], v[164:167], off nt

; DI unsigned cvt_pk_bf16(float lo, float hi) { unsigned r; asm volatile("v_cvt_pk_bf16_f32 %0, %1, %2" : "=v"(r) : "v"(lo), "v"(hi)); return r; }
;     DI void operator()(const f32x4 (&acc)[2][2][4][2], const pg8::Unit& u, int wr, int wc, int fr, int fq) const {
;     ...
;                         const int row = row0 + ai * 128 + m * 16, b = row >> 11, s = row & 2047;
;                         const int pos = ((s & ((1 << sh) - 1)) << (11 - sh)) + (s >> sh);
;                         float v[8];
; #pragma unroll
;                         for (int e = 0; e < 4; ++e) { v[e] = acc[ai][bj][m][0][e]; v[4 + e] = acc[ai][bj][m][1][e]; }
;                         if (kind < 2) {
;                             const float sc = (kind == 0) ? 0.08838834764831845f : 1.0f;
;                             u32x4 w; w.x = pg8::cvt_pk_bf16(v[0] * sc, v[1] * sc); w.y = pg8::cvt_pk_bf16(v[2] * sc, v[3] * sc); w.z = pg8::cvt_pk_bf16(v[4] * sc, v[5] * sc); w.w = pg8::cvt_pk_bf16(v[6] * sc, v[7] * sc);
;                             bf16_t* base = (bf16_t*)(ws + (kind == 0 ? WS_QB : WS_KB));
;                             const size_t o = ((size_t)((b * 12 + head) * 64 + (pos >> 5)) * 8 + (cw >> 4)) * 512 + (size_t)(((pos & 31) + 32 * ((cw >> 3) & 1)) * 8);
;                             if (NOSTORE) asm volatile("" :: "v"(w)); else st16_stream(base + o, w);
.LBB0_113:
	v_and_or_b32 v5, v5, 31, v174
	s_andn2_b64 vcc, exec, s[12:13]
	v_lshlrev_b32_e32 v8, 4, v5
	s_cbranch_vccnz .LBB0_115
	v_mul_f32_e32 v5, v3, v128
	v_mul_f32_e32 v7, v3, v129
	v_cvt_pk_bf16_f32 v164, v5, v7
	v_mul_f32_e32 v5, v3, v130
	v_mul_f32_e32 v7, v3, v131
	v_cvt_pk_bf16_f32 v165, v5, v7
	v_mul_f32_e32 v5, v3, v124
	s_add_u32 s10, s18, s14
	v_ashrrev_i32_e32 v11, 31, v10
	v_mul_f32_e32 v7, v3, v125
	v_cvt_pk_bf16_f32 v166, v5, v7
	v_mul_f32_e32 v5, v3, v126
	s_addc_u32 s11, s19, 0
	v_lshlrev_b64 v[10:11], 13, v[10:11]
	v_mul_f32_e32 v7, v3, v127
	v_cvt_pk_bf16_f32 v167, v5, v7
	v_lshl_add_u64 v[10:11], s[10:11], 0, v[10:11]
	v_mov_b32_e32 v5, v2
	v_lshl_add_u64 v[10:11], v[10:11], 0, v[4:5]
	v_mov_b32_e32 v9, v2
	v_lshl_add_u64 v[10:11], v[10:11], 0, v[8:9]
	global_store_dwordx4 v[10:11], v[164:167], off nt

; DI unsigned cvt_pk_bf16(float lo, float hi) { unsigned r; asm volatile("v_cvt_pk_bf16_f32 %0, %1, %2" : "=v"(r) : "v"(lo), "v"(hi)); return r; }
;     DI void operator()(const f32x4 (&acc)[2][2][4][2], const pg8::Unit& u, int wr, int wc, int fr, int fq) const {
;     ...
;                         const int row = row0 + ai * 128 + m * 16, b = row >> 11, s = row & 2047;
;                         const int pos = ((s & ((1 << sh) - 1)) << (11 - sh)) + (s >> sh);
;                         float v[8];
; #pragma unroll
;                         for (int e = 0; e < 4; ++e) { v[e] = acc[ai][bj][m][0][e]; v[4 + e] = acc[ai][bj][m][1][e]; }
;                         if (kind < 2) {
;                             const float sc = (kind == 0) ? 0.08838834764831845f : 1.0f;
;                             u32x4 w; w.x = pg8::cvt_pk_bf16(v[0] * sc, v[1] * sc); w.y = pg8::cvt_pk_bf16(v[2] * sc, v[3] * sc); w.z = pg8::cvt_pk_bf16(v[4] * sc, v[5] * sc); w.w = pg8::cvt_pk_bf16(v[6] * sc, v[7] * sc);
;                             bf16_t* base = (bf16_t*)(ws + (kind == 0 ? WS_QB : WS_KB));
;                             const size_t o = ((size_t)((b * 12 + head) * 64 + (pos >> 5)) * 8 + (cw >> 4)) * 512 + (size_t)(((pos & 31) + 32 * ((cw >> 3) & 1)) * 8);
;                             if (NOSTORE) asm volatile("" :: "v"(w)); else st16_stream(base + o, w);
.LBB0_117:
	v_and_or_b32 v5, v5, 31, v174
	s_andn2_b64 vcc, exec, s[10:11]
	v_lshlrev_b32_e32 v10, 4, v5
	s_cbranch_vccnz .LBB0_119
	v_mul_f32_e32 v5, v3, v120
	v_mul_f32_e32 v7, v3, v121
	v_cvt_pk_bf16_f32 v164, v5, v7
	v_mul_f32_e32 v5, v3, v122
	v_mul_f32_e32 v7, v3, v123
	v_cvt_pk_bf16_f32 v165, v5, v7
	v_mul_f32_e32 v5, v3, v116
	s_add_u32 s10, s18, s14
	v_ashrrev_i32_e32 v161, 31, v160
	v_mul_f32_e32 v7, v3, v117
	v_cvt_pk_bf16_f32 v166, v5, v7
	v_mul_f32_e32 v5, v3, v118
	s_addc_u32 s11, s19, 0
	v_lshlrev_b64 v[160:161], 13, v[160:161]
	v_mul_f32_e32 v7, v3, v119
	v_cvt_pk_bf16_f32 v167, v5, v7
	v_lshl_add_u64 v[160:161], s[10:11], 0, v[160:161]
	v_mov_b32_e32 v5, v2
	v_lshl_add_u64 v[160:161], v[160:161], 0, v[4:5]
	v_mov_b32_e32 v11, v2
	v_lshl_add_u64 v[160:161], v[160:161], 0, v[10:11]
	global_store_dwordx4 v[160:161], v[164:167], off nt

; DI unsigned cvt_pk_bf16(float lo, float hi) { unsigned r; asm volatile("v_cvt_pk_bf16_f32 %0, %1, %2" : "=v"(r) : "v"(lo), "v"(hi)); return r; }
;     DI void operator()(const f32x4 (&acc)[2][2][4][2], const pg8::Unit& u, int wr, int wc, int fr, int fq) const {
;     ...
;                         const int row = row0 + ai * 128 + m * 16, b = row >> 11, s = row & 2047;
;                         const int pos = ((s & ((1 << sh) - 1)) << (11 - sh)) + (s >> sh);
;                         float v[8];
; #pragma unroll
;                         for (int e = 0; e < 4; ++e) { v[e] = acc[ai][bj][m][0][e]; v[4 + e] = acc[ai][bj][m][1][e]; }
;                         if (kind < 2) {
;                             const float sc = (kind == 0) ? 0.08838834764831845f : 1.0f;
;                             u32x4 w; w.x = pg8::cvt_pk_bf16(v[0] * sc, v[1] * sc); w.y = pg8::cvt_pk_bf16(v[2] * sc, v[3] * sc); w.z = pg8::cvt_pk_bf16(v[4] * sc, v[5] * sc); w.w = pg8::cvt_pk_bf16(v[6] * sc, v[7] * sc);
;                             bf16_t* base = (bf16_t*)(ws + (kind == 0 ? WS_QB : WS_KB));
;                             const size_t o = ((size_t)((b * 12 + head) * 64 + (pos >> 5)) * 8 + (cw >> 4)) * 512 + (size_t)(((pos & 31) + 32 * ((cw >> 3) & 1)) * 8);
;                             if (NOSTORE) asm volatile("" :: "v"(w)); else st16_stream(base + o, w);
.LBB0_121:
	v_and_or_b32 v5, v5, 31, v174
	s_andn2_b64 vcc, exec, s[10:11]
	v_lshlrev_b32_e32 v160, 4, v5
	s_cbranch_vccnz .LBB0_123
	v_mul_f32_e32 v5, v3, v112
	v_mul_f32_e32 v7, v3, v113
	v_cvt_pk_bf16_f32 v164, v5, v7
	v_mul_f32_e32 v5, v3, v114
	v_mul_f32_e32 v7, v3, v115
	v_cvt_pk_bf16_f32 v165, v5, v7
	v_mul_f32_e32 v5, v3, v108
	s_add_u32 s10, s18, s14
	v_ashrrev_i32_e32 v163, 31, v162
	v_mul_f32_e32 v7, v3, v109
	v_cvt_pk_bf16_f32 v166, v5, v7
	v_mul_f32_e32 v5, v3, v110
	s_addc_u32 s11, s19, 0
	v_lshlrev_b64 v[162:163], 13, v[162:163]
	v_mul_f32_e32 v7, v3, v111
	v_cvt_pk_bf16_f32 v167, v5, v7
	v_lshl_add_u64 v[162:163], s[10:11], 0, v[162:163]
	v_mov_b32_e32 v5, v2
	v_lshl_add_u64 v[162:163], v[162:163], 0, v[4:5]
	v_mov_b32_e32 v161, v2
	v_lshl_add_u64 v[162:163], v[162:163], 0, v[160:161]
	global_store_dwordx4 v[162:163], v[164:167], off nt

; DI unsigned cvt_pk_bf16(float lo, float hi) { unsigned r; asm volatile("v_cvt_pk_bf16_f32 %0, %1, %2" : "=v"(r) : "v"(lo), "v"(hi)); return r; }
;     DI void operator()(const f32x4 (&acc)[2][2][4][2], const pg8::Unit& u, int wr, int wc, int fr, int fq) const {
;     ...
;                         const int row = row0 + ai * 128 + m * 16, b = row >> 11, s = row & 2047;
;                         const int pos = ((s & ((1 << sh) - 1)) << (11 - sh)) + (s >> sh);
;                         float v[8];
; #pragma unroll
;                         for (int e = 0; e < 4; ++e) { v[e] = acc[ai][bj][m][0][e]; v[4 + e] = acc[ai][bj][m][1][e]; }
;                         if (kind < 2) {
;                             const float sc = (kind == 0) ? 0.08838834764831845f : 1.0f;
;                             u32x4 w; w.x = pg8::cvt_pk_bf16(v[0] * sc, v[1] * sc); w.y = pg8::cvt_pk_bf16(v[2] * sc, v[3] * sc); w.z = pg8::cvt_pk_bf16(v[4] * sc, v[5] * sc); w.w = pg8::cvt_pk_bf16(v[6] * sc, v[7] * sc);
;                             bf16_t* base = (bf16_t*)(ws + (kind == 0 ? WS_QB : WS_KB));
;                             const size_t o = ((size_t)((b * 12 + head) * 64 + (pos >> 5)) * 8 + (cw >> 4)) * 512 + (size_t)(((pos & 31) + 32 * ((cw >> 3) & 1)) * 8);
;                             if (NOSTORE) asm volatile("" :: "v"(w)); else st16_stream(base + o, w);
.LBB0_125:
	v_and_or_b32 v5, v5, 31, v174
	s_andn2_b64 vcc, exec, s[10:11]
	v_lshlrev_b32_e32 v162, 4, v5
	s_cbranch_vccnz .LBB0_127
	v_mul_f32_e32 v5, v3, v104
	v_mul_f32_e32 v11, v3, v105
	v_cvt_pk_bf16_f32 v166, v5, v11
	v_mul_f32_e32 v5, v3, v106
	v_mul_f32_e32 v11, v3, v107
	v_cvt_pk_bf16_f32 v167, v5, v11
	v_mul_f32_e32 v5, v3, v100
	s_add_u32 s10, s18, s14
	v_ashrrev_i32_e32 v165, 31, v164
	v_mul_f32_e32 v11, v3, v101
	v_cvt_pk_bf16_f32 v168, v5, v11
	v_mul_f32_e32 v5, v3, v102
	s_addc_u32 s11, s19, 0
	v_lshlrev_b64 v[164:165], 13, v[164:165]
	v_mul_f32_e32 v11, v3, v103
	v_cvt_pk_bf16_f32 v169, v5, v11
	v_lshl_add_u64 v[164:165], s[10:11], 0, v[164:165]
	v_mov_b32_e32 v5, v2
	v_lshl_add_u64 v[164:165], v[164:165], 0, v[4:5]
	v_mov_b32_e32 v163, v2
	v_lshl_add_u64 v[164:165], v[164:165], 0, v[162:163]
	global_store_dwordx4 v[164:165], v[166:169], off nt

; DI unsigned cvt_pk_bf16(float lo, float hi) { unsigned r; asm volatile("v_cvt_pk_bf16_f32 %0, %1, %2" : "=v"(r) : "v"(lo), "v"(hi)); return r; }
;     DI void operator()(const f32x4 (&acc)[2][2][4][2], const pg8::Unit& u, int wr, int wc, int fr, int fq) const {
;     ...
;                         const int row = row0 + ai * 128 + m * 16, b = row >> 11, s = row & 2047;
;                         const int pos = ((s & ((1 << sh) - 1)) << (11 - sh)) + (s >> sh);
;                         float v[8];
; #pragma unroll
;                         for (int e = 0; e < 4; ++e) { v[e] = acc[ai][bj][m][0][e]; v[4 + e] = acc[ai][bj][m][1][e]; }
;                         if (kind < 2) {
;                             const float sc = (kind == 0) ? 0.08838834764831845f : 1.0f;
;                             u32x4 w; w.x = pg8::cvt_pk_bf16(v[0] * sc, v[1] * sc); w.y = pg8::cvt_pk_bf16(v[2] * sc, v[3] * sc); w.z = pg8::cvt_pk_bf16(v[4] * sc, v[5] * sc); w.w = pg8::cvt_pk_bf16(v[6] * sc, v[7] * sc);
;                             bf16_t* base = (bf16_t*)(ws + (kind == 0 ? WS_QB : WS_KB));
;                             const size_t o = ((size_t)((b * 12 + head) * 64 + (pos >> 5)) * 8 + (cw >> 4)) * 512 + (size_t)(((pos & 31) + 32 * ((cw >> 3) & 1)) * 8);
;                             if (NOSTORE) asm volatile("" :: "v"(w)); else st16_stream(base + o, w);
.LBB0_129:
	v_and_or_b32 v5, v5, 31, v174
	s_andn2_b64 vcc, exec, s[10:11]
	v_lshlrev_b32_e32 v164, 4, v5
	s_cbranch_vccnz .LBB0_131
	v_mul_f32_e32 v5, v3, v96
	v_mul_f32_e32 v11, v3, v97
	v_cvt_pk_bf16_f32 v168, v5, v11
	v_mul_f32_e32 v5, v3, v98
	v_mul_f32_e32 v11, v3, v99
	v_cvt_pk_bf16_f32 v169, v5, v11
	v_mul_f32_e32 v5, v3, v92
	s_add_u32 s10, s18, s14
	v_ashrrev_i32_e32 v167, 31, v166
	v_mul_f32_e32 v11, v3, v93
	v_cvt_pk_bf16_f32 v170, v5, v11
	v_mul_f32_e32 v5, v3, v94
	s_addc_u32 s11, s19, 0
	v_lshlrev_b64 v[166:167], 13, v[166:167]
	v_mul_f32_e32 v11, v3, v95
	v_cvt_pk_bf16_f32 v171, v5, v11
	v_lshl_add_u64 v[166:167], s[10:11], 0, v[166:167]
	v_mov_b32_e32 v5, v2
	v_lshl_add_u64 v[166:167], v[166:167], 0, v[4:5]
	v_mov_b32_e32 v165, v2
	v_lshl_add_u64 v[166:167], v[166:167], 0, v[164:165]
	global_store_dwordx4 v[166:167], v[168:171], off nt

; DI unsigned cvt_pk_bf16(float lo, float hi) { unsigned r; asm volatile("v_cvt_pk_bf16_f32 %0, %1, %2" : "=v"(r) : "v"(lo), "v"(hi)); return r; }
;     DI void operator()(const f32x4 (&acc)[2][2][4][2], const pg8::Unit& u, int wr, int wc, int fr, int fq) const {
;     ...
;                         const int row = row0 + ai * 128 + m * 16, b = row >> 11, s = row & 2047;
;                         const int pos = ((s & ((1 << sh) - 1)) << (11 - sh)) + (s >> sh);
;                         float v[8];
; #pragma unroll
;                         for (int e = 0; e < 4; ++e) { v[e] = acc[ai][bj][m][0][e]; v[4 + e] = acc[ai][bj][m][1][e]; }
;                         if (kind < 2) {
;                             const float sc = (kind == 0) ? 0.08838834764831845f : 1.0f;
;                             u32x4 w; w.x = pg8::cvt_pk_bf16(v[0] * sc, v[1] * sc); w.y = pg8::cvt_pk_bf16(v[2] * sc, v[3] * sc); w.z = pg8::cvt_pk_bf16(v[4] * sc, v[5] * sc); w.w = pg8::cvt_pk_bf16(v[6] * sc, v[7] * sc);
;                             bf16_t* base = (bf16_t*)(ws + (kind == 0 ? WS_QB : WS_KB));
;                             const size_t o = ((size_t)((b * 12 + head) * 64 + (pos >> 5)) * 8 + (cw >> 4)) * 512 + (size_t)(((pos & 31) + 32 * ((cw >> 3) & 1)) * 8);
;                             if (NOSTORE) asm volatile("" :: "v"(w)); else st16_stream(base + o, w);
.LBB0_133:
	v_and_or_b32 v5, v5, 31, v174
	s_andn2_b64 vcc, exec, s[10:11]
	v_lshlrev_b32_e32 v166, 4, v5
	s_cbranch_vccnz .LBB0_135
	v_mul_f32_e32 v5, v3, v88
	v_mul_f32_e32 v11, v3, v89
	v_cvt_pk_bf16_f32 v210, v5, v11
	v_mul_f32_e32 v5, v3, v90
	v_mul_f32_e32 v11, v3, v91
	v_cvt_pk_bf16_f32 v211, v5, v11
	v_mul_f32_e32 v5, v3, v84
	s_add_u32 s10, s18, s14
	v_ashrrev_i32_e32 v169, 31, v168
	v_mul_f32_e32 v11, v3, v85
	v_cvt_pk_bf16_f32 v212, v5, v11
	v_mul_f32_e32 v5, v3, v86
	s_addc_u32 s11, s19, 0
	v_lshlrev_b64 v[168:169], 13, v[168:169]
	v_mul_f32_e32 v11, v3, v87
	v_cvt_pk_bf16_f32 v213, v5, v11
	v_lshl_add_u64 v[168:169], s[10:11], 0, v[168:169]
	v_mov_b32_e32 v5, v2
	v_lshl_add_u64 v[168:169], v[168:169], 0, v[4:5]
	v_mov_b32_e32 v167, v2
	v_lshl_add_u64 v[168:169], v[168:169], 0, v[166:167]
	global_store_dwordx4 v[168:169], v[210:213], off nt

; DI unsigned cvt_pk_bf16(float lo, float hi) { unsigned r; asm volatile("v_cvt_pk_bf16_f32 %0, %1, %2" : "=v"(r) : "v"(lo), "v"(hi)); return r; }
;     DI void operator()(const f32x4 (&acc)[2][2][4][2], const pg8::Unit& u, int wr, int wc, int fr, int fq) const {
;     ...
;                         const int row = row0 + ai * 128 + m * 16, b = row >> 11, s = row & 2047;
;                         const int pos = ((s & ((1 << sh) - 1)) << (11 - sh)) + (s >> sh);
;                         float v[8];
; #pragma unroll
;                         for (int e = 0; e < 4; ++e) { v[e] = acc[ai][bj][m][0][e]; v[4 + e] = acc[ai][bj][m][1][e]; }
;                         if (kind < 2) {
;                             const float sc = (kind == 0) ? 0.08838834764831845f : 1.0f;
;                             u32x4 w; w.x = pg8::cvt_pk_bf16(v[0] * sc, v[1] * sc); w.y = pg8::cvt_pk_bf16(v[2] * sc, v[3] * sc); w.z = pg8::cvt_pk_bf16(v[4] * sc, v[5] * sc); w.w = pg8::cvt_pk_bf16(v[6] * sc, v[7] * sc);
;                             bf16_t* base = (bf16_t*)(ws + (kind == 0 ? WS_QB : WS_KB));
;                             const size_t o = ((size_t)((b * 12 + head) * 64 + (pos >> 5)) * 8 + (cw >> 4)) * 512 + (size_t)(((pos & 31) + 32 * ((cw >> 3) & 1)) * 8);
;                             if (NOSTORE) asm volatile("" :: "v"(w)); else st16_stream(base + o, w);
.LBB0_137:
	v_and_or_b32 v5, v5, 31, v174
	s_andn2_b64 vcc, exec, s[10:11]
	v_lshlrev_b32_e32 v168, 4, v5
	s_cbranch_vccnz .LBB0_139
	v_mul_f32_e32 v5, v3, v80
	v_mul_f32_e32 v7, v3, v81
	v_cvt_pk_bf16_f32 v212, v5, v7
	v_mul_f32_e32 v5, v3, v82
	v_mul_f32_e32 v7, v3, v83
	v_cvt_pk_bf16_f32 v213, v5, v7
	v_mul_f32_e32 v5, v3, v76
	s_add_u32 s10, s18, s14
	v_ashrrev_i32_e32 v171, 31, v170
	v_mul_f32_e32 v7, v3, v77
	v_cvt_pk_bf16_f32 v214, v5, v7
	v_mul_f32_e32 v5, v3, v78
	s_addc_u32 s11, s19, 0
	v_lshlrev_b64 v[170:171], 13, v[170:171]
	v_mul_f32_e32 v7, v3, v79
	v_cvt_pk_bf16_f32 v215, v5, v7
	v_lshl_add_u64 v[170:171], s[10:11], 0, v[170:171]
	v_mov_b32_e32 v5, v2
	v_lshl_add_u64 v[170:171], v[170:171], 0, v[4:5]
	v_mov_b32_e32 v169, v2
	v_lshl_add_u64 v[170:171], v[170:171], 0, v[168:169]
	global_store_dwordx4 v[170:171], v[212:215], off nt

; DI unsigned cvt_pk_bf16(float lo, float hi) { unsigned r; asm volatile("v_cvt_pk_bf16_f32 %0, %1, %2" : "=v"(r) : "v"(lo), "v"(hi)); return r; }
;     DI void operator()(const f32x4 (&acc)[2][2][4][2], const pg8::Unit& u, int wr, int wc, int fr, int fq) const {
;     ...
;                         const int row = row0 + ai * 128 + m * 16, b = row >> 11, s = row & 2047;
;                         const int pos = ((s & ((1 << sh) - 1)) << (11 - sh)) + (s >> sh);
;                         float v[8];
; #pragma unroll
;                         for (int e = 0; e < 4; ++e) { v[e] = acc[ai][bj][m][0][e]; v[4 + e] = acc[ai][bj][m][1][e]; }
;                         if (kind < 2) {
;                             const float sc = (kind == 0) ? 0.08838834764831845f : 1.0f;
;                             u32x4 w; w.x = pg8::cvt_pk_bf16(v[0] * sc, v[1] * sc); w.y = pg8::cvt_pk_bf16(v[2] * sc, v[3] * sc); w.z = pg8::cvt_pk_bf16(v[4] * sc, v[5] * sc); w.w = pg8::cvt_pk_bf16(v[6] * sc, v[7] * sc);
;                             bf16_t* base = (bf16_t*)(ws + (kind == 0 ? WS_QB : WS_KB));
;                             const size_t o = ((size_t)((b * 12 + head) * 64 + (pos >> 5)) * 8 + (cw >> 4)) * 512 + (size_t)(((pos & 31) + 32 * ((cw >> 3) & 1)) * 8);
;                             if (NOSTORE) asm volatile("" :: "v"(w)); else st16_stream(base + o, w);
.LBB0_154:
	v_mul_f32_e32 v5, v3, v72
	v_mul_f32_e32 v7, v3, v73
	v_cvt_pk_bf16_f32 v212, v5, v7
	v_mul_f32_e32 v5, v3, v74
	v_mul_f32_e32 v7, v3, v75
	v_cvt_pk_bf16_f32 v213, v5, v7
	v_mul_f32_e32 v5, v3, v68
	s_add_u32 s10, s18, s14
	v_ashrrev_i32_e32 v171, 31, v170
	v_mul_f32_e32 v7, v3, v69
	v_cvt_pk_bf16_f32 v214, v5, v7
	v_mul_f32_e32 v5, v3, v70
	s_addc_u32 s11, s19, 0
	v_lshlrev_b64 v[170:171], 13, v[170:171]
	v_mul_f32_e32 v7, v3, v71
	v_cvt_pk_bf16_f32 v215, v5, v7
	v_lshl_add_u64 v[170:171], s[10:11], 0, v[170:171]
	v_mov_b32_e32 v5, v2
	v_lshl_add_u64 v[170:171], v[170:171], 0, v[4:5]
	v_mov_b32_e32 v7, v2
	v_lshl_add_u64 v[6:7], v[170:171], 0, v[6:7]
	global_store_dwordx4 v[6:7], v[212:215], off nt
	s_mov_b64 s[10:11], -1
	s_and_b64 vcc, exec, s[4:5]
	v_add_u32_e32 v6, s13, v187
	s_cbranch_vccz .LBB0_142

; DI unsigned cvt_pk_bf16(float lo, float hi) { unsigned r; asm volatile("v_cvt_pk_bf16_f32 %0, %1, %2" : "=v"(r) : "v"(lo), "v"(hi)); return r; }
;     DI void operator()(const f32x4 (&acc)[2][2][4][2], const pg8::Unit& u, int wr, int wc, int fr, int fq) const {
;     ...
;                         const int row = row0 + ai * 128 + m * 16, b = row >> 11, s = row & 2047;
;                         const int pos = ((s & ((1 << sh) - 1)) << (11 - sh)) + (s >> sh);
;                         float v[8];
; #pragma unroll
;                         for (int e = 0; e < 4; ++e) { v[e] = acc[ai][bj][m][0][e]; v[4 + e] = acc[ai][bj][m][1][e]; }
;                         if (kind < 2) {
;                             const float sc = (kind == 0) ? 0.08838834764831845f : 1.0f;
;                             u32x4 w; w.x = pg8::cvt_pk_bf16(v[0] * sc, v[1] * sc); w.y = pg8::cvt_pk_bf16(v[2] * sc, v[3] * sc); w.z = pg8::cvt_pk_bf16(v[4] * sc, v[5] * sc); w.w = pg8::cvt_pk_bf16(v[6] * sc, v[7] * sc);
;                             bf16_t* base = (bf16_t*)(ws + (kind == 0 ? WS_QB : WS_KB));
;                             const size_t o = ((size_t)((b * 12 + head) * 64 + (pos >> 5)) * 8 + (cw >> 4)) * 512 + (size_t)(((pos & 31) + 32 * ((cw >> 3) & 1)) * 8);
;                             if (NOSTORE) asm volatile("" :: "v"(w)); else st16_stream(base + o, w);
.LBB0_156:
	v_mul_f32_e32 v7, v3, v65
	v_mul_f32_e32 v5, v3, v64
	v_cvt_pk_bf16_f32 v180, v5, v7
	v_mul_f32_e32 v7, v3, v67
	v_mul_f32_e32 v5, v3, v66
	v_cvt_pk_bf16_f32 v181, v5, v7
	v_mul_f32_e32 v7, v3, v61
	v_mul_f32_e32 v5, v3, v60
	v_cvt_pk_bf16_f32 v182, v5, v7
	v_mul_f32_e32 v7, v3, v63
	v_mul_f32_e32 v5, v3, v62
	v_cvt_pk_bf16_f32 v183, v5, v7
	s_add_u32 s10, s18, s14
	v_ashrrev_i32_e32 v7, 31, v6
	s_addc_u32 s11, s19, 0
	v_lshlrev_b64 v[6:7], 13, v[6:7]
	v_lshl_add_u64 v[6:7], s[10:11], 0, v[6:7]
	v_mov_b32_e32 v5, v2
	v_lshl_add_u64 v[6:7], v[6:7], 0, v[4:5]
	v_mov_b32_e32 v9, v2
	v_lshl_add_u64 v[6:7], v[6:7], 0, v[8:9]
	global_store_dwordx4 v[6:7], v[180:183], off nt
	s_mov_b64 s[10:11], -1
	s_and_b64 vcc, exec, s[4:5]
	v_add_u32_e32 v6, s13, v191
	s_cbranch_vccz .LBB0_144

; DI unsigned cvt_pk_bf16(float lo, float hi) { unsigned r; asm volatile("v_cvt_pk_bf16_f32 %0, %1, %2" : "=v"(r) : "v"(lo), "v"(hi)); return r; }
;     DI void operator()(const f32x4 (&acc)[2][2][4][2], const pg8::Unit& u, int wr, int wc, int fr, int fq) const {
;     ...
;                         const int row = row0 + ai * 128 + m * 16, b = row >> 11, s = row & 2047;
;                         const int pos = ((s & ((1 << sh) - 1)) << (11 - sh)) + (s >> sh);
;                         float v[8];
; #pragma unroll
;                         for (int e = 0; e < 4; ++e) { v[e] = acc[ai][bj][m][0][e]; v[4 + e] = acc[ai][bj][m][1][e]; }
;                         if (kind < 2) {
;                             const float sc = (kind == 0) ? 0.08838834764831845f : 1.0f;
;                             u32x4 w; w.x = pg8::cvt_pk_bf16(v[0] * sc, v[1] * sc); w.y = pg8::cvt_pk_bf16(v[2] * sc, v[3] * sc); w.z = pg8::cvt_pk_bf16(v[4] * sc, v[5] * sc); w.w = pg8::cvt_pk_bf16(v[6] * sc, v[7] * sc);
;                             bf16_t* base = (bf16_t*)(ws + (kind == 0 ? WS_QB : WS_KB));
;                             const size_t o = ((size_t)((b * 12 + head) * 64 + (pos >> 5)) * 8 + (cw >> 4)) * 512 + (size_t)(((pos & 31) + 32 * ((cw >> 3) & 1)) * 8);
;                             if (NOSTORE) asm volatile("" :: "v"(w)); else st16_stream(base + o, w);
.LBB0_158:
	v_mul_f32_e32 v7, v3, v57
	v_mul_f32_e32 v5, v3, v56
	v_cvt_pk_bf16_f32 v180, v5, v7
	v_mul_f32_e32 v7, v3, v59
	v_mul_f32_e32 v5, v3, v58
	v_cvt_pk_bf16_f32 v181, v5, v7
	v_mul_f32_e32 v7, v3, v53
	v_mul_f32_e32 v5, v3, v52
	v_cvt_pk_bf16_f32 v182, v5, v7
	v_mul_f32_e32 v7, v3, v55
	v_mul_f32_e32 v5, v3, v54
	v_cvt_pk_bf16_f32 v183, v5, v7
	s_add_u32 s10, s18, s14
	v_ashrrev_i32_e32 v7, 31, v6
	s_addc_u32 s11, s19, 0
	v_lshlrev_b64 v[6:7], 13, v[6:7]
	v_lshl_add_u64 v[6:7], s[10:11], 0, v[6:7]
	v_mov_b32_e32 v5, v2
	v_lshl_add_u64 v[6:7], v[6:7], 0, v[4:5]
	v_mov_b32_e32 v11, v2
	v_lshl_add_u64 v[6:7], v[6:7], 0, v[10:11]
	global_store_dwordx4 v[6:7], v[180:183], off nt
	s_mov_b64 s[10:11], -1
	s_and_b64 vcc, exec, s[4:5]
	v_add_u32_e32 v6, s13, v194
	s_cbranch_vccz .LBB0_146

; DI unsigned cvt_pk_bf16(float lo, float hi) { unsigned r; asm volatile("v_cvt_pk_bf16_f32 %0, %1, %2" : "=v"(r) : "v"(lo), "v"(hi)); return r; }
;     DI void operator()(const f32x4 (&acc)[2][2][4][2], const pg8::Unit& u, int wr, int wc, int fr, int fq) const {
;     ...
;                         const int row = row0 + ai * 128 + m * 16, b = row >> 11, s = row & 2047;
;                         const int pos = ((s & ((1 << sh) - 1)) << (11 - sh)) + (s >> sh);
;                         float v[8];
; #pragma unroll
;                         for (int e = 0; e < 4; ++e) { v[e] = acc[ai][bj][m][0][e]; v[4 + e] = acc[ai][bj][m][1][e]; }
;                         if (kind < 2) {
;                             const float sc = (kind == 0) ? 0.08838834764831845f : 1.0f;
;                             u32x4 w; w.x = pg8::cvt_pk_bf16(v[0] * sc, v[1] * sc); w.y = pg8::cvt_pk_bf16(v[2] * sc, v[3] * sc); w.z = pg8::cvt_pk_bf16(v[4] * sc, v[5] * sc); w.w = pg8::cvt_pk_bf16(v[6] * sc, v[7] * sc);
;                             bf16_t* base = (bf16_t*)(ws + (kind == 0 ? WS_QB : WS_KB));
;                             const size_t o = ((size_t)((b * 12 + head) * 64 + (pos >> 5)) * 8 + (cw >> 4)) * 512 + (size_t)(((pos & 31) + 32 * ((cw >> 3) & 1)) * 8);
;                             if (NOSTORE) asm volatile("" :: "v"(w)); else st16_stream(base + o, w);
.LBB0_160:
	v_mul_f32_e32 v7, v3, v49
	v_mul_f32_e32 v5, v3, v48
	v_cvt_pk_bf16_f32 v8, v5, v7
	v_mul_f32_e32 v7, v3, v51
	v_mul_f32_e32 v5, v3, v50
	v_cvt_pk_bf16_f32 v9, v5, v7
	v_mul_f32_e32 v7, v3, v45
	v_mul_f32_e32 v5, v3, v44
	v_cvt_pk_bf16_f32 v10, v5, v7
	v_mul_f32_e32 v7, v3, v47
	v_mul_f32_e32 v5, v3, v46
	v_cvt_pk_bf16_f32 v11, v5, v7
	s_add_u32 s10, s18, s14
	v_ashrrev_i32_e32 v7, 31, v6
	s_addc_u32 s11, s19, 0
	v_lshlrev_b64 v[6:7], 13, v[6:7]
	v_lshl_add_u64 v[6:7], s[10:11], 0, v[6:7]
	v_mov_b32_e32 v5, v2
	v_lshl_add_u64 v[6:7], v[6:7], 0, v[4:5]
	v_mov_b32_e32 v161, v2
	v_lshl_add_u64 v[6:7], v[6:7], 0, v[160:161]
	global_store_dwordx4 v[6:7], v[8:11], off nt

; DI unsigned cvt_pk_bf16(float lo, float hi) { unsigned r; asm volatile("v_cvt_pk_bf16_f32 %0, %1, %2" : "=v"(r) : "v"(lo), "v"(hi)); return r; }
;     DI void operator()(const f32x4 (&acc)[2][2][4][2], const pg8::Unit& u, int wr, int wc, int fr, int fq) const {
;     ...
;                         const int row = row0 + ai * 128 + m * 16, b = row >> 11, s = row & 2047;
;                         const int pos = ((s & ((1 << sh) - 1)) << (11 - sh)) + (s >> sh);
;                         float v[8];
; #pragma unroll
;                         for (int e = 0; e < 4; ++e) { v[e] = acc[ai][bj][m][0][e]; v[4 + e] = acc[ai][bj][m][1][e]; }
;                         if (kind < 2) {
;                             const float sc = (kind == 0) ? 0.08838834764831845f : 1.0f;
;                             u32x4 w; w.x = pg8::cvt_pk_bf16(v[0] * sc, v[1] * sc); w.y = pg8::cvt_pk_bf16(v[2] * sc, v[3] * sc); w.z = pg8::cvt_pk_bf16(v[4] * sc, v[5] * sc); w.w = pg8::cvt_pk_bf16(v[6] * sc, v[7] * sc);
;                             bf16_t* base = (bf16_t*)(ws + (kind == 0 ? WS_QB : WS_KB));
;                             const size_t o = ((size_t)((b * 12 + head) * 64 + (pos >> 5)) * 8 + (cw >> 4)) * 512 + (size_t)(((pos & 31) + 32 * ((cw >> 3) & 1)) * 8);
;                             if (NOSTORE) asm volatile("" :: "v"(w)); else st16_stream(base + o, w);
.LBB0_170:
	v_mul_f32_e32 v7, v3, v41
	v_mul_f32_e32 v5, v3, v40
	v_cvt_pk_bf16_f32 v180, v5, v7
	v_mul_f32_e32 v7, v3, v43
	v_mul_f32_e32 v5, v3, v42
	v_cvt_pk_bf16_f32 v181, v5, v7
	v_mul_f32_e32 v7, v3, v37
	v_mul_f32_e32 v5, v3, v36
	v_cvt_pk_bf16_f32 v182, v5, v7
	v_mul_f32_e32 v7, v3, v39
	v_mul_f32_e32 v5, v3, v38
	v_cvt_pk_bf16_f32 v183, v5, v7
	s_add_u32 s10, s18, s14
	v_ashrrev_i32_e32 v7, 31, v6
	s_addc_u32 s11, s19, 0
	v_lshlrev_b64 v[6:7], 13, v[6:7]
	v_lshl_add_u64 v[6:7], s[10:11], 0, v[6:7]
	v_mov_b32_e32 v5, v2
	v_lshl_add_u64 v[6:7], v[6:7], 0, v[4:5]
	v_mov_b32_e32 v163, v2
	v_lshl_add_u64 v[6:7], v[6:7], 0, v[162:163]
	global_store_dwordx4 v[6:7], v[180:183], off nt
	s_mov_b64 s[10:11], -1
	s_and_b64 vcc, exec, s[4:5]
	v_add_u32_e32 v6, v204, v8
	s_cbranch_vccz .LBB0_164

; DI unsigned cvt_pk_bf16(float lo, float hi) { unsigned r; asm volatile("v_cvt_pk_bf16_f32 %0, %1, %2" : "=v"(r) : "v"(lo), "v"(hi)); return r; }
;     DI void operator()(const f32x4 (&acc)[2][2][4][2], const pg8::Unit& u, int wr, int wc, int fr, int fq) const {
;     ...
;                         const int row = row0 + ai * 128 + m * 16, b = row >> 11, s = row & 2047;
;                         const int pos = ((s & ((1 << sh) - 1)) << (11 - sh)) + (s >> sh);
;                         float v[8];
; #pragma unroll
;                         for (int e = 0; e < 4; ++e) { v[e] = acc[ai][bj][m][0][e]; v[4 + e] = acc[ai][bj][m][1][e]; }
;                         if (kind < 2) {
;                             const float sc = (kind == 0) ? 0.08838834764831845f : 1.0f;
;                             u32x4 w; w.x = pg8::cvt_pk_bf16(v[0] * sc, v[1] * sc); w.y = pg8::cvt_pk_bf16(v[2] * sc, v[3] * sc); w.z = pg8::cvt_pk_bf16(v[4] * sc, v[5] * sc); w.w = pg8::cvt_pk_bf16(v[6] * sc, v[7] * sc);
;                             bf16_t* base = (bf16_t*)(ws + (kind == 0 ? WS_QB : WS_KB));
;                             const size_t o = ((size_t)((b * 12 + head) * 64 + (pos >> 5)) * 8 + (cw >> 4)) * 512 + (size_t)(((pos & 31) + 32 * ((cw >> 3) & 1)) * 8);
;                             if (NOSTORE) asm volatile("" :: "v"(w)); else st16_stream(base + o, w);
.LBB0_172:
	v_mul_f32_e32 v7, v3, v33
	v_mul_f32_e32 v5, v3, v32
	v_cvt_pk_bf16_f32 v160, v5, v7
	v_mul_f32_e32 v7, v3, v35
	v_mul_f32_e32 v5, v3, v34
	v_cvt_pk_bf16_f32 v161, v5, v7
	v_mul_f32_e32 v7, v3, v29
	v_mul_f32_e32 v5, v3, v28
	v_cvt_pk_bf16_f32 v162, v5, v7
	v_mul_f32_e32 v7, v3, v31
	v_mul_f32_e32 v5, v3, v30
	v_cvt_pk_bf16_f32 v163, v5, v7
	s_add_u32 s10, s18, s14
	v_ashrrev_i32_e32 v7, 31, v6
	s_addc_u32 s11, s19, 0
	v_lshlrev_b64 v[6:7], 13, v[6:7]
	v_lshl_add_u64 v[6:7], s[10:11], 0, v[6:7]
	v_mov_b32_e32 v5, v2
	v_lshl_add_u64 v[6:7], v[6:7], 0, v[4:5]
	v_mov_b32_e32 v165, v2
	v_lshl_add_u64 v[6:7], v[6:7], 0, v[164:165]
	global_store_dwordx4 v[6:7], v[160:163], off nt
	s_mov_b64 s[10:11], -1
	s_and_b64 vcc, exec, s[4:5]
	v_add_u32_e32 v6, v208, v8
	s_cbranch_vccz .LBB0_166

; DI unsigned cvt_pk_bf16(float lo, float hi) { unsigned r; asm volatile("v_cvt_pk_bf16_f32 %0, %1, %2" : "=v"(r) : "v"(lo), "v"(hi)); return r; }
;     DI void operator()(const f32x4 (&acc)[2][2][4][2], const pg8::Unit& u, int wr, int wc, int fr, int fq) const {
;     ...
;                         const int row = row0 + ai * 128 + m * 16, b = row >> 11, s = row & 2047;
;                         const int pos = ((s & ((1 << sh) - 1)) << (11 - sh)) + (s >> sh);
;                         float v[8];
; #pragma unroll
;                         for (int e = 0; e < 4; ++e) { v[e] = acc[ai][bj][m][0][e]; v[4 + e] = acc[ai][bj][m][1][e]; }
;                         if (kind < 2) {
;                             const float sc = (kind == 0) ? 0.08838834764831845f : 1.0f;
;                             u32x4 w; w.x = pg8::cvt_pk_bf16(v[0] * sc, v[1] * sc); w.y = pg8::cvt_pk_bf16(v[2] * sc, v[3] * sc); w.z = pg8::cvt_pk_bf16(v[4] * sc, v[5] * sc); w.w = pg8::cvt_pk_bf16(v[6] * sc, v[7] * sc);
;                             bf16_t* base = (bf16_t*)(ws + (kind == 0 ? WS_QB : WS_KB));
;                             const size_t o = ((size_t)((b * 12 + head) * 64 + (pos >> 5)) * 8 + (cw >> 4)) * 512 + (size_t)(((pos & 31) + 32 * ((cw >> 3) & 1)) * 8);
;                             if (NOSTORE) asm volatile("" :: "v"(w)); else st16_stream(base + o, w);
.LBB0_174:
	v_mul_f32_e32 v7, v3, v25
	v_mul_f32_e32 v5, v3, v24
	v_cvt_pk_bf16_f32 v160, v5, v7
	v_mul_f32_e32 v7, v3, v27
	v_mul_f32_e32 v5, v3, v26
	v_cvt_pk_bf16_f32 v161, v5, v7
	v_mul_f32_e32 v7, v3, v21
	v_mul_f32_e32 v5, v3, v20
	v_cvt_pk_bf16_f32 v162, v5, v7
	v_mul_f32_e32 v7, v3, v23
	v_mul_f32_e32 v5, v3, v22
	v_cvt_pk_bf16_f32 v163, v5, v7
	s_add_u32 s10, s18, s14
	v_ashrrev_i32_e32 v7, 31, v6
	s_addc_u32 s11, s19, 0
	v_lshlrev_b64 v[6:7], 13, v[6:7]
	v_lshl_add_u64 v[6:7], s[10:11], 0, v[6:7]
	v_mov_b32_e32 v5, v2
	v_lshl_add_u64 v[6:7], v[6:7], 0, v[4:5]
	v_mov_b32_e32 v167, v2
	v_lshl_add_u64 v[6:7], v[6:7], 0, v[166:167]
	global_store_dwordx4 v[6:7], v[160:163], off nt
	s_mov_b64 s[10:11], -1
	s_and_b64 vcc, exec, s[4:5]
	v_add_u32_e32 v6, v211, v8
	s_cbranch_vccz .LBB0_168

; DI unsigned cvt_pk_bf16(float lo, float hi) { unsigned r; asm volatile("v_cvt_pk_bf16_f32 %0, %1, %2" : "=v"(r) : "v"(lo), "v"(hi)); return r; }
;     DI void operator()(const f32x4 (&acc)[2][2][4][2], const pg8::Unit& u, int wr, int wc, int fr, int fq) const {
;     ...
;                         const int row = row0 + ai * 128 + m * 16, b = row >> 11, s = row & 2047;
;                         const int pos = ((s & ((1 << sh) - 1)) << (11 - sh)) + (s >> sh);
;                         float v[8];
; #pragma unroll
;                         for (int e = 0; e < 4; ++e) { v[e] = acc[ai][bj][m][0][e]; v[4 + e] = acc[ai][bj][m][1][e]; }
;                         if (kind < 2) {
;                             const float sc = (kind == 0) ? 0.08838834764831845f : 1.0f;
;                             u32x4 w; w.x = pg8::cvt_pk_bf16(v[0] * sc, v[1] * sc); w.y = pg8::cvt_pk_bf16(v[2] * sc, v[3] * sc); w.z = pg8::cvt_pk_bf16(v[4] * sc, v[5] * sc); w.w = pg8::cvt_pk_bf16(v[6] * sc, v[7] * sc);
;                             bf16_t* base = (bf16_t*)(ws + (kind == 0 ? WS_QB : WS_KB));
;                             const size_t o = ((size_t)((b * 12 + head) * 64 + (pos >> 5)) * 8 + (cw >> 4)) * 512 + (size_t)(((pos & 31) + 32 * ((cw >> 3) & 1)) * 8);
;                             if (NOSTORE) asm volatile("" :: "v"(w)); else st16_stream(base + o, w);
.LBB0_176:
	v_mul_f32_e32 v7, v3, v17
	v_mul_f32_e32 v5, v3, v16
	v_cvt_pk_bf16_f32 v8, v5, v7
	v_mul_f32_e32 v7, v3, v19
	v_mul_f32_e32 v5, v3, v18
	v_cvt_pk_bf16_f32 v9, v5, v7
	v_mul_f32_e32 v7, v3, v13
	v_mul_f32_e32 v5, v3, v12
	v_cvt_pk_bf16_f32 v10, v5, v7
	s_add_u32 s4, s18, s14
	v_ashrrev_i32_e32 v7, 31, v6
	v_mul_f32_e32 v5, v3, v14
	s_addc_u32 s5, s19, 0
	v_lshlrev_b64 v[6:7], 13, v[6:7]
	v_mul_f32_e32 v3, v3, v15
	v_cvt_pk_bf16_f32 v11, v5, v3
	v_lshl_add_u64 v[6:7], s[4:5], 0, v[6:7]
	v_mov_b32_e32 v5, v2
	v_lshl_add_u64 v[4:5], v[6:7], 0, v[4:5]
	v_mov_b32_e32 v169, v2
	v_lshl_add_u64 v[4:5], v[4:5], 0, v[168:169]
	global_store_dwordx4 v[4:5], v[8:11], off nt

; DI float sigmoidf_(float x) { return __builtin_amdgcn_rcpf(1.0f + __expf(-x)); }
; DI unsigned cvt_pk_bf16(float lo, float hi) { unsigned r; asm volatile("v_cvt_pk_bf16_f32 %0, %1, %2" : "=v"(r) : "v"(lo), "v"(hi)); return r; }
;     DI void operator()(const f32x4 (&acc)[2][2][4][2], const pg8::Unit& u, int wr, int wc, int fr, int fq) const {
;     ...
; #pragma unroll
;                 for (int ai = 0; ai < 2; ++ai)
; #pragma unroll
;                     for (int m = 0; m < 4; ++m) {
;                         const int row = row0 + ai * 128 + m * 16;
;                         float v[8];
; #pragma unroll
;                         for (int e = 0; e < 4; ++e) { v[e] = acc[ai][bj][m][0][e]; v[4 + e] = acc[ai][bj][m][1][e]; }
;                         if (mode == 1) {
; #pragma unroll
;                             for (int e = 0; e < 8; ++e) v[e] = __logf(lb[e] + (1.0f - lb[e]) * sigmoidf_(v[e]));
;                         } else if (mode == 2) {
; #pragma unroll
;                             for (int e = 0; e < 8; ++e) v[e] = sigmoidf_(v[e]);
;                         }
;                         u32x4 w; w.x = pg8::cvt_pk_bf16(v[0], v[1]); w.y = pg8::cvt_pk_bf16(v[2], v[3]); w.z = pg8::cvt_pk_bf16(v[4], v[5]); w.w = pg8::cvt_pk_bf16(v[6], v[7]);
;                         if (NOSTORE) asm volatile("" :: "v"(w)); else st16_stream(base + (size_t)row * D + col, w);
;                     }
.LBB0_198:
	s_add_u32 s56, s18, s14
	s_addc_u32 s57, s19, s15
	v_cvt_pk_bf16_f32 v136, v159, v171
	v_ashrrev_i32_e32 v159, 31, v158
	v_lshl_add_u64 v[134:135], v[162:163], 1, s[56:57]
	v_lshlrev_b64 v[132:133], 12, v[158:159]
	v_cvt_pk_bf16_f32 v137, v180, v181
	v_lshl_add_u64 v[180:181], v[134:135], 0, v[132:133]
	v_cvt_pk_bf16_f32 v138, v182, v183
	v_cvt_pk_bf16_f32 v139, v184, v185
	global_store_dwordx4 v[180:181], v[136:139], off nt
	s_andn2_b64 vcc, exec, s[16:17]
	s_mov_b64 s[10:11], -1
	v_cndmask_b32_e64 v136, 0, 1, s[16:17]
	v_cmp_ne_u32_e64 s[6:7], 1, v136
	s_cbranch_vccnz .LBB0_201
	s_and_b64 vcc, exec, s[4:5]
	s_cbranch_vccnz .LBB0_240
	v_mul_f32_e32 v136, 0xbfb8aa3b, v128
	v_mul_f32_e32 v137, 0xbfb8aa3b, v129
	v_mul_f32_e32 v138, 0xbfb8aa3b, v130
	v_mul_f32_e32 v139, 0xbfb8aa3b, v131
	v_mul_f32_e32 v163, 0xbfb8aa3b, v124
	v_mul_f32_e32 v171, 0xbfb8aa3b, v125
	v_mul_f32_e32 v180, 0xbfb8aa3b, v126
	v_mul_f32_e32 v181, 0xbfb8aa3b, v127
	v_exp_f32_e32 v136, v136
	v_exp_f32_e32 v137, v137
	v_exp_f32_e32 v138, v138
	v_exp_f32_e32 v139, v139
	v_exp_f32_e32 v163, v163
	v_exp_f32_e32 v171, v171
	v_exp_f32_e32 v180, v180
	v_exp_f32_e32 v181, v181
	v_add_f32_e32 v136, 1.0, v136
	v_add_f32_e32 v137, 1.0, v137
	v_add_f32_e32 v138, 1.0, v138
	v_add_f32_e32 v139, 1.0, v139
	v_add_f32_e32 v163, 1.0, v163
	v_add_f32_e32 v171, 1.0, v171
	v_add_f32_e32 v180, 1.0, v180
	v_add_f32_e32 v181, 1.0, v181
	v_rcp_f32_e32 v136, v136
	v_rcp_f32_e32 v137, v137
	v_rcp_f32_e32 v138, v138
	v_rcp_f32_e32 v139, v139
	v_rcp_f32_e32 v163, v163
	v_rcp_f32_e32 v171, v171
	v_rcp_f32_e32 v180, v180
	v_rcp_f32_e32 v181, v181
	s_mov_b64 s[10:11], 0

; DI float sigmoidf_(float x) { return __builtin_amdgcn_rcpf(1.0f + __expf(-x)); }
; DI unsigned cvt_pk_bf16(float lo, float hi) { unsigned r; asm volatile("v_cvt_pk_bf16_f32 %0, %1, %2" : "=v"(r) : "v"(lo), "v"(hi)); return r; }
;     DI void operator()(const f32x4 (&acc)[2][2][4][2], const pg8::Unit& u, int wr, int wc, int fr, int fq) const {
;     ...
; #pragma unroll
;                 for (int ai = 0; ai < 2; ++ai)
; #pragma unroll
;                     for (int m = 0; m < 4; ++m) {
;                         const int row = row0 + ai * 128 + m * 16;
;                         float v[8];
; #pragma unroll
;                         for (int e = 0; e < 4; ++e) { v[e] = acc[ai][bj][m][0][e]; v[4 + e] = acc[ai][bj][m][1][e]; }
;                         if (mode == 1) {
; #pragma unroll
;                             for (int e = 0; e < 8; ++e) v[e] = __logf(lb[e] + (1.0f - lb[e]) * sigmoidf_(v[e]));
;                         } else if (mode == 2) {
; #pragma unroll
;                             for (int e = 0; e < 8; ++e) v[e] = sigmoidf_(v[e]);
;                         }
;                         u32x4 w; w.x = pg8::cvt_pk_bf16(v[0], v[1]); w.y = pg8::cvt_pk_bf16(v[2], v[3]); w.z = pg8::cvt_pk_bf16(v[4], v[5]); w.w = pg8::cvt_pk_bf16(v[6], v[7]);
;                         if (NOSTORE) asm volatile("" :: "v"(w)); else st16_stream(base + (size_t)row * D + col, w);
;                     }
.LBB0_203:
	v_or_b32_e32 v124, 16, v158
	v_ashrrev_i32_e32 v125, 31, v124
	v_lshlrev_b64 v[124:125], 12, v[124:125]
	v_cvt_pk_bf16_f32 v126, v136, v137
	v_cvt_pk_bf16_f32 v127, v138, v139
	v_cvt_pk_bf16_f32 v128, v163, v171
	v_cvt_pk_bf16_f32 v129, v180, v181
	v_lshl_add_u64 v[130:131], v[134:135], 0, v[124:125]
	s_and_b64 vcc, exec, s[6:7]
	s_mov_b64 s[10:11], -1
	global_store_dwordx4 v[130:131], v[126:129], off nt
	s_cbranch_vccnz .LBB0_206
	s_and_b64 vcc, exec, s[4:5]
	s_cbranch_vccnz .LBB0_241
	v_mul_f32_e32 v126, 0xbfb8aa3b, v120
	v_mul_f32_e32 v127, 0xbfb8aa3b, v121
	v_mul_f32_e32 v128, 0xbfb8aa3b, v122
	v_mul_f32_e32 v129, 0xbfb8aa3b, v123
	v_mul_f32_e32 v130, 0xbfb8aa3b, v116
	v_mul_f32_e32 v131, 0xbfb8aa3b, v117
	v_mul_f32_e32 v136, 0xbfb8aa3b, v118
	v_mul_f32_e32 v137, 0xbfb8aa3b, v119
	v_exp_f32_e32 v126, v126
	v_exp_f32_e32 v127, v127
	v_exp_f32_e32 v128, v128
	v_exp_f32_e32 v129, v129
	v_exp_f32_e32 v130, v130
	v_exp_f32_e32 v131, v131
	v_exp_f32_e32 v136, v136
	v_exp_f32_e32 v137, v137
	v_add_f32_e32 v126, 1.0, v126
	v_add_f32_e32 v127, 1.0, v127
	v_add_f32_e32 v128, 1.0, v128
	v_add_f32_e32 v129, 1.0, v129
	v_add_f32_e32 v130, 1.0, v130
	v_add_f32_e32 v131, 1.0, v131
	v_add_f32_e32 v136, 1.0, v136
	v_add_f32_e32 v137, 1.0, v137
	v_rcp_f32_e32 v126, v126
	v_rcp_f32_e32 v127, v127
	v_rcp_f32_e32 v128, v128
	v_rcp_f32_e32 v129, v129
	v_rcp_f32_e32 v130, v130
	v_rcp_f32_e32 v131, v131
	v_rcp_f32_e32 v136, v136
	v_rcp_f32_e32 v137, v137
	s_mov_b64 s[10:11], 0

; DI float sigmoidf_(float x) { return __builtin_amdgcn_rcpf(1.0f + __expf(-x)); }
; DI unsigned cvt_pk_bf16(float lo, float hi) { unsigned r; asm volatile("v_cvt_pk_bf16_f32 %0, %1, %2" : "=v"(r) : "v"(lo), "v"(hi)); return r; }
;     DI void operator()(const f32x4 (&acc)[2][2][4][2], const pg8::Unit& u, int wr, int wc, int fr, int fq) const {
;     ...
; #pragma unroll
;                 for (int ai = 0; ai < 2; ++ai)
; #pragma unroll
;                     for (int m = 0; m < 4; ++m) {
;                         const int row = row0 + ai * 128 + m * 16;
;                         float v[8];
; #pragma unroll
;                         for (int e = 0; e < 4; ++e) { v[e] = acc[ai][bj][m][0][e]; v[4 + e] = acc[ai][bj][m][1][e]; }
;                         if (mode == 1) {
; #pragma unroll
;                             for (int e = 0; e < 8; ++e) v[e] = __logf(lb[e] + (1.0f - lb[e]) * sigmoidf_(v[e]));
;                         } else if (mode == 2) {
; #pragma unroll
;                             for (int e = 0; e < 8; ++e) v[e] = sigmoidf_(v[e]);
;                         }
;                         u32x4 w; w.x = pg8::cvt_pk_bf16(v[0], v[1]); w.y = pg8::cvt_pk_bf16(v[2], v[3]); w.z = pg8::cvt_pk_bf16(v[4], v[5]); w.w = pg8::cvt_pk_bf16(v[6], v[7]);
;                         if (NOSTORE) asm volatile("" :: "v"(w)); else st16_stream(base + (size_t)row * D + col, w);
;                     }
.LBB0_208:
	v_or_b32_e32 v116, 32, v158
	v_ashrrev_i32_e32 v117, 31, v116
	v_lshlrev_b64 v[116:117], 12, v[116:117]
	v_cvt_pk_bf16_f32 v118, v126, v127
	v_cvt_pk_bf16_f32 v119, v128, v129
	v_cvt_pk_bf16_f32 v120, v130, v131
	v_cvt_pk_bf16_f32 v121, v136, v137
	v_lshl_add_u64 v[122:123], v[134:135], 0, v[116:117]
	s_and_b64 vcc, exec, s[6:7]
	s_mov_b64 s[10:11], -1
	global_store_dwordx4 v[122:123], v[118:121], off nt
	s_cbranch_vccnz .LBB0_211
	s_and_b64 vcc, exec, s[4:5]
	s_cbranch_vccnz .LBB0_242
	v_mul_f32_e32 v118, 0xbfb8aa3b, v112
	v_mul_f32_e32 v119, 0xbfb8aa3b, v113
	v_mul_f32_e32 v120, 0xbfb8aa3b, v114
	v_mul_f32_e32 v121, 0xbfb8aa3b, v115
	v_mul_f32_e32 v122, 0xbfb8aa3b, v108
	v_mul_f32_e32 v123, 0xbfb8aa3b, v109
	v_mul_f32_e32 v126, 0xbfb8aa3b, v110
	v_mul_f32_e32 v127, 0xbfb8aa3b, v111
	v_exp_f32_e32 v118, v118
	v_exp_f32_e32 v119, v119
	v_exp_f32_e32 v120, v120
	v_exp_f32_e32 v121, v121
	v_exp_f32_e32 v122, v122
	v_exp_f32_e32 v123, v123
	v_exp_f32_e32 v126, v126
	v_exp_f32_e32 v127, v127
	v_add_f32_e32 v118, 1.0, v118
	v_add_f32_e32 v119, 1.0, v119
	v_add_f32_e32 v120, 1.0, v120
	v_add_f32_e32 v121, 1.0, v121
	v_add_f32_e32 v122, 1.0, v122
	v_add_f32_e32 v123, 1.0, v123
	v_add_f32_e32 v126, 1.0, v126
	v_add_f32_e32 v127, 1.0, v127
	v_rcp_f32_e32 v118, v118
	v_rcp_f32_e32 v119, v119
	v_rcp_f32_e32 v120, v120
	v_rcp_f32_e32 v121, v121
	v_rcp_f32_e32 v122, v122
	v_rcp_f32_e32 v123, v123
	v_rcp_f32_e32 v126, v126
	v_rcp_f32_e32 v127, v127
	s_mov_b64 s[10:11], 0

; DI float sigmoidf_(float x) { return __builtin_amdgcn_rcpf(1.0f + __expf(-x)); }
; DI unsigned cvt_pk_bf16(float lo, float hi) { unsigned r; asm volatile("v_cvt_pk_bf16_f32 %0, %1, %2" : "=v"(r) : "v"(lo), "v"(hi)); return r; }
;     DI void operator()(const f32x4 (&acc)[2][2][4][2], const pg8::Unit& u, int wr, int wc, int fr, int fq) const {
;     ...
; #pragma unroll
;                 for (int ai = 0; ai < 2; ++ai)
; #pragma unroll
;                     for (int m = 0; m < 4; ++m) {
;                         const int row = row0 + ai * 128 + m * 16;
;                         float v[8];
; #pragma unroll
;                         for (int e = 0; e < 4; ++e) { v[e] = acc[ai][bj][m][0][e]; v[4 + e] = acc[ai][bj][m][1][e]; }
;                         if (mode == 1) {
; #pragma unroll
;                             for (int e = 0; e < 8; ++e) v[e] = __logf(lb[e] + (1.0f - lb[e]) * sigmoidf_(v[e]));
;                         } else if (mode == 2) {
; #pragma unroll
;                             for (int e = 0; e < 8; ++e) v[e] = sigmoidf_(v[e]);
;                         }
;                         u32x4 w; w.x = pg8::cvt_pk_bf16(v[0], v[1]); w.y = pg8::cvt_pk_bf16(v[2], v[3]); w.z = pg8::cvt_pk_bf16(v[4], v[5]); w.w = pg8::cvt_pk_bf16(v[6], v[7]);
;                         if (NOSTORE) asm volatile("" :: "v"(w)); else st16_stream(base + (size_t)row * D + col, w);
;                     }
.LBB0_213:
	v_or_b32_e32 v108, 48, v158
	v_ashrrev_i32_e32 v109, 31, v108
	v_lshlrev_b64 v[108:109], 12, v[108:109]
	v_cvt_pk_bf16_f32 v110, v118, v119
	v_cvt_pk_bf16_f32 v111, v120, v121
	v_cvt_pk_bf16_f32 v112, v122, v123
	v_cvt_pk_bf16_f32 v113, v126, v127
	v_lshl_add_u64 v[114:115], v[134:135], 0, v[108:109]
	s_and_b64 vcc, exec, s[6:7]
	s_mov_b64 s[10:11], -1
	global_store_dwordx4 v[114:115], v[110:113], off nt
	s_cbranch_vccnz .LBB0_216
	s_and_b64 vcc, exec, s[4:5]
	s_cbranch_vccnz .LBB0_243
	v_mul_f32_e32 v110, 0xbfb8aa3b, v104
	v_mul_f32_e32 v111, 0xbfb8aa3b, v105
	v_mul_f32_e32 v112, 0xbfb8aa3b, v106
	v_mul_f32_e32 v113, 0xbfb8aa3b, v107
	v_mul_f32_e32 v114, 0xbfb8aa3b, v100
	v_mul_f32_e32 v115, 0xbfb8aa3b, v101
	v_mul_f32_e32 v118, 0xbfb8aa3b, v102
	v_mul_f32_e32 v119, 0xbfb8aa3b, v103
	v_exp_f32_e32 v110, v110
	v_exp_f32_e32 v111, v111
	v_exp_f32_e32 v112, v112
	v_exp_f32_e32 v113, v113
	v_exp_f32_e32 v114, v114
	v_exp_f32_e32 v115, v115
	v_exp_f32_e32 v118, v118
	v_exp_f32_e32 v119, v119
	v_add_f32_e32 v110, 1.0, v110
	v_add_f32_e32 v111, 1.0, v111
	v_add_f32_e32 v112, 1.0, v112
	v_add_f32_e32 v113, 1.0, v113
	v_add_f32_e32 v114, 1.0, v114
	v_add_f32_e32 v115, 1.0, v115
	v_add_f32_e32 v118, 1.0, v118
	v_add_f32_e32 v119, 1.0, v119
	v_rcp_f32_e32 v110, v110
	v_rcp_f32_e32 v111, v111
	v_rcp_f32_e32 v112, v112
	v_rcp_f32_e32 v113, v113
	v_rcp_f32_e32 v114, v114
	v_rcp_f32_e32 v115, v115
	v_rcp_f32_e32 v118, v118
	v_rcp_f32_e32 v119, v119
	s_mov_b64 s[10:11], 0

; DI float sigmoidf_(float x) { return __builtin_amdgcn_rcpf(1.0f + __expf(-x)); }
; DI unsigned cvt_pk_bf16(float lo, float hi) { unsigned r; asm volatile("v_cvt_pk_bf16_f32 %0, %1, %2" : "=v"(r) : "v"(lo), "v"(hi)); return r; }
;     DI void operator()(const f32x4 (&acc)[2][2][4][2], const pg8::Unit& u, int wr, int wc, int fr, int fq) const {
;     ...
; #pragma unroll
;                 for (int ai = 0; ai < 2; ++ai)
; #pragma unroll
;                     for (int m = 0; m < 4; ++m) {
;                         const int row = row0 + ai * 128 + m * 16;
;                         float v[8];
; #pragma unroll
;                         for (int e = 0; e < 4; ++e) { v[e] = acc[ai][bj][m][0][e]; v[4 + e] = acc[ai][bj][m][1][e]; }
;                         if (mode == 1) {
; #pragma unroll
;                             for (int e = 0; e < 8; ++e) v[e] = __logf(lb[e] + (1.0f - lb[e]) * sigmoidf_(v[e]));
;                         } else if (mode == 2) {
; #pragma unroll
;                             for (int e = 0; e < 8; ++e) v[e] = sigmoidf_(v[e]);
;                         }
;                         u32x4 w; w.x = pg8::cvt_pk_bf16(v[0], v[1]); w.y = pg8::cvt_pk_bf16(v[2], v[3]); w.z = pg8::cvt_pk_bf16(v[4], v[5]); w.w = pg8::cvt_pk_bf16(v[6], v[7]);
;                         if (NOSTORE) asm volatile("" :: "v"(w)); else st16_stream(base + (size_t)row * D + col, w);
;                     }
.LBB0_218:
	v_lshlrev_b64 v[100:101], 12, v[158:159]
	v_lshl_add_u64 v[100:101], v[100:101], 0, s[24:25]
	v_cvt_pk_bf16_f32 v102, v110, v111
	v_cvt_pk_bf16_f32 v103, v112, v113
	v_cvt_pk_bf16_f32 v104, v114, v115
	v_cvt_pk_bf16_f32 v105, v118, v119
	v_lshl_add_u64 v[106:107], v[134:135], 0, v[100:101]
	s_and_b64 vcc, exec, s[6:7]
	s_mov_b64 s[10:11], -1
	global_store_dwordx4 v[106:107], v[102:105], off nt
	s_cbranch_vccnz .LBB0_221
	s_and_b64 vcc, exec, s[4:5]
	s_cbranch_vccnz .LBB0_244
	v_mul_f32_e32 v102, 0xbfb8aa3b, v96
	v_mul_f32_e32 v103, 0xbfb8aa3b, v97
	v_mul_f32_e32 v104, 0xbfb8aa3b, v98
	v_mul_f32_e32 v105, 0xbfb8aa3b, v99
	v_mul_f32_e32 v106, 0xbfb8aa3b, v92
	v_mul_f32_e32 v107, 0xbfb8aa3b, v93
	v_mul_f32_e32 v110, 0xbfb8aa3b, v94
	v_mul_f32_e32 v111, 0xbfb8aa3b, v95
	v_exp_f32_e32 v102, v102
	v_exp_f32_e32 v103, v103
	v_exp_f32_e32 v104, v104
	v_exp_f32_e32 v105, v105
	v_exp_f32_e32 v106, v106
	v_exp_f32_e32 v107, v107
	v_exp_f32_e32 v110, v110
	v_exp_f32_e32 v111, v111
	v_add_f32_e32 v102, 1.0, v102
	v_add_f32_e32 v103, 1.0, v103
	v_add_f32_e32 v104, 1.0, v104
	v_add_f32_e32 v105, 1.0, v105
	v_add_f32_e32 v106, 1.0, v106
	v_add_f32_e32 v107, 1.0, v107
	v_add_f32_e32 v110, 1.0, v110
	v_add_f32_e32 v111, 1.0, v111
	v_rcp_f32_e32 v102, v102
	v_rcp_f32_e32 v103, v103
	v_rcp_f32_e32 v104, v104
	v_rcp_f32_e32 v105, v105
	v_rcp_f32_e32 v106, v106
	v_rcp_f32_e32 v107, v107
	v_rcp_f32_e32 v110, v110
	v_rcp_f32_e32 v111, v111
	s_mov_b64 s[10:11], 0

; DI float sigmoidf_(float x) { return __builtin_amdgcn_rcpf(1.0f + __expf(-x)); }
; DI unsigned cvt_pk_bf16(float lo, float hi) { unsigned r; asm volatile("v_cvt_pk_bf16_f32 %0, %1, %2" : "=v"(r) : "v"(lo), "v"(hi)); return r; }
;     DI void operator()(const f32x4 (&acc)[2][2][4][2], const pg8::Unit& u, int wr, int wc, int fr, int fq) const {
;     ...
; #pragma unroll
;                 for (int ai = 0; ai < 2; ++ai)
; #pragma unroll
;                     for (int m = 0; m < 4; ++m) {
;                         const int row = row0 + ai * 128 + m * 16;
;                         float v[8];
; #pragma unroll
;                         for (int e = 0; e < 4; ++e) { v[e] = acc[ai][bj][m][0][e]; v[4 + e] = acc[ai][bj][m][1][e]; }
;                         if (mode == 1) {
; #pragma unroll
;                             for (int e = 0; e < 8; ++e) v[e] = __logf(lb[e] + (1.0f - lb[e]) * sigmoidf_(v[e]));
;                         } else if (mode == 2) {
; #pragma unroll
;                             for (int e = 0; e < 8; ++e) v[e] = sigmoidf_(v[e]);
;                         }
;                         u32x4 w; w.x = pg8::cvt_pk_bf16(v[0], v[1]); w.y = pg8::cvt_pk_bf16(v[2], v[3]); w.z = pg8::cvt_pk_bf16(v[4], v[5]); w.w = pg8::cvt_pk_bf16(v[6], v[7]);
;                         if (NOSTORE) asm volatile("" :: "v"(w)); else st16_stream(base + (size_t)row * D + col, w);
;                     }
.LBB0_223:
	v_lshlrev_b64 v[92:93], 12, v[158:159]
	v_lshl_add_u64 v[92:93], v[92:93], 0, s[40:41]
	v_cvt_pk_bf16_f32 v94, v102, v103
	v_cvt_pk_bf16_f32 v95, v104, v105
	v_cvt_pk_bf16_f32 v96, v106, v107
	v_cvt_pk_bf16_f32 v97, v110, v111
	v_lshl_add_u64 v[98:99], v[134:135], 0, v[92:93]
	s_and_b64 vcc, exec, s[6:7]
	s_mov_b64 s[10:11], -1
	global_store_dwordx4 v[98:99], v[94:97], off nt
	s_cbranch_vccnz .LBB0_226
	s_and_b64 vcc, exec, s[4:5]
	s_cbranch_vccnz .LBB0_245
	v_mul_f32_e32 v94, 0xbfb8aa3b, v88
	v_mul_f32_e32 v95, 0xbfb8aa3b, v89
	v_mul_f32_e32 v96, 0xbfb8aa3b, v90
	v_mul_f32_e32 v97, 0xbfb8aa3b, v91
	v_mul_f32_e32 v98, 0xbfb8aa3b, v84
	v_mul_f32_e32 v99, 0xbfb8aa3b, v85
	v_mul_f32_e32 v102, 0xbfb8aa3b, v86
	v_mul_f32_e32 v103, 0xbfb8aa3b, v87
	v_exp_f32_e32 v94, v94
	v_exp_f32_e32 v95, v95
	v_exp_f32_e32 v96, v96
	v_exp_f32_e32 v97, v97
	v_exp_f32_e32 v98, v98
	v_exp_f32_e32 v99, v99
	v_exp_f32_e32 v102, v102
	v_exp_f32_e32 v103, v103
	v_add_f32_e32 v94, 1.0, v94
	v_add_f32_e32 v95, 1.0, v95
	v_add_f32_e32 v96, 1.0, v96
	v_add_f32_e32 v97, 1.0, v97
	v_add_f32_e32 v98, 1.0, v98
	v_add_f32_e32 v99, 1.0, v99
	v_add_f32_e32 v102, 1.0, v102
	v_add_f32_e32 v103, 1.0, v103
	v_rcp_f32_e32 v94, v94
	v_rcp_f32_e32 v95, v95
	v_rcp_f32_e32 v96, v96
	v_rcp_f32_e32 v97, v97
	v_rcp_f32_e32 v98, v98
	v_rcp_f32_e32 v99, v99
	v_rcp_f32_e32 v102, v102
	v_rcp_f32_e32 v103, v103
	s_mov_b64 s[10:11], 0

; DI float sigmoidf_(float x) { return __builtin_amdgcn_rcpf(1.0f + __expf(-x)); }
; DI unsigned cvt_pk_bf16(float lo, float hi) { unsigned r; asm volatile("v_cvt_pk_bf16_f32 %0, %1, %2" : "=v"(r) : "v"(lo), "v"(hi)); return r; }
;     DI void operator()(const f32x4 (&acc)[2][2][4][2], const pg8::Unit& u, int wr, int wc, int fr, int fq) const {
;     ...
; #pragma unroll
;                 for (int ai = 0; ai < 2; ++ai)
; #pragma unroll
;                     for (int m = 0; m < 4; ++m) {
;                         const int row = row0 + ai * 128 + m * 16;
;                         float v[8];
; #pragma unroll
;                         for (int e = 0; e < 4; ++e) { v[e] = acc[ai][bj][m][0][e]; v[4 + e] = acc[ai][bj][m][1][e]; }
;                         if (mode == 1) {
; #pragma unroll
;                             for (int e = 0; e < 8; ++e) v[e] = __logf(lb[e] + (1.0f - lb[e]) * sigmoidf_(v[e]));
;                         } else if (mode == 2) {
; #pragma unroll
;                             for (int e = 0; e < 8; ++e) v[e] = sigmoidf_(v[e]);
;                         }
;                         u32x4 w; w.x = pg8::cvt_pk_bf16(v[0], v[1]); w.y = pg8::cvt_pk_bf16(v[2], v[3]); w.z = pg8::cvt_pk_bf16(v[4], v[5]); w.w = pg8::cvt_pk_bf16(v[6], v[7]);
;                         if (NOSTORE) asm volatile("" :: "v"(w)); else st16_stream(base + (size_t)row * D + col, w);
;                     }
.LBB0_228:
	v_lshlrev_b64 v[84:85], 12, v[158:159]
	v_lshl_add_u64 v[84:85], v[84:85], 0, s[42:43]
	v_cvt_pk_bf16_f32 v86, v94, v95
	v_cvt_pk_bf16_f32 v87, v96, v97
	v_cvt_pk_bf16_f32 v88, v98, v99
	v_cvt_pk_bf16_f32 v89, v102, v103
	v_lshl_add_u64 v[90:91], v[134:135], 0, v[84:85]
	s_and_b64 vcc, exec, s[6:7]
	s_mov_b64 s[10:11], -1
	global_store_dwordx4 v[90:91], v[86:89], off nt
	s_cbranch_vccnz .LBB0_231
	s_and_b64 vcc, exec, s[4:5]
	s_cbranch_vccnz .LBB0_246
	v_mul_f32_e32 v86, 0xbfb8aa3b, v80
	v_mul_f32_e32 v87, 0xbfb8aa3b, v81
	v_mul_f32_e32 v88, 0xbfb8aa3b, v82
	v_mul_f32_e32 v89, 0xbfb8aa3b, v83
	v_mul_f32_e32 v90, 0xbfb8aa3b, v76
	v_mul_f32_e32 v91, 0xbfb8aa3b, v77
	v_mul_f32_e32 v94, 0xbfb8aa3b, v78
	v_mul_f32_e32 v95, 0xbfb8aa3b, v79
	v_exp_f32_e32 v86, v86
	v_exp_f32_e32 v87, v87
	v_exp_f32_e32 v88, v88
	v_exp_f32_e32 v89, v89
	v_exp_f32_e32 v90, v90
	v_exp_f32_e32 v91, v91
	v_exp_f32_e32 v94, v94
	v_exp_f32_e32 v95, v95
	v_add_f32_e32 v86, 1.0, v86
	v_add_f32_e32 v87, 1.0, v87
	v_add_f32_e32 v88, 1.0, v88
	v_add_f32_e32 v89, 1.0, v89
	v_add_f32_e32 v90, 1.0, v90
	v_add_f32_e32 v91, 1.0, v91
	v_add_f32_e32 v94, 1.0, v94
	v_add_f32_e32 v95, 1.0, v95
	v_rcp_f32_e32 v86, v86
	v_rcp_f32_e32 v87, v87
	v_rcp_f32_e32 v88, v88
	v_rcp_f32_e32 v89, v89
	v_rcp_f32_e32 v90, v90
	v_rcp_f32_e32 v91, v91
	v_rcp_f32_e32 v94, v94
	v_rcp_f32_e32 v95, v95
	s_mov_b64 s[10:11], 0

; DI float sigmoidf_(float x) { return __builtin_amdgcn_rcpf(1.0f + __expf(-x)); }
; DI unsigned cvt_pk_bf16(float lo, float hi) { unsigned r; asm volatile("v_cvt_pk_bf16_f32 %0, %1, %2" : "=v"(r) : "v"(lo), "v"(hi)); return r; }
;     DI void operator()(const f32x4 (&acc)[2][2][4][2], const pg8::Unit& u, int wr, int wc, int fr, int fq) const {
;     ...
; #pragma unroll
;                 for (int ai = 0; ai < 2; ++ai)
; #pragma unroll
;                     for (int m = 0; m < 4; ++m) {
;                         const int row = row0 + ai * 128 + m * 16;
;                         float v[8];
; #pragma unroll
;                         for (int e = 0; e < 4; ++e) { v[e] = acc[ai][bj][m][0][e]; v[4 + e] = acc[ai][bj][m][1][e]; }
;                         if (mode == 1) {
; #pragma unroll
;                             for (int e = 0; e < 8; ++e) v[e] = __logf(lb[e] + (1.0f - lb[e]) * sigmoidf_(v[e]));
;                         } else if (mode == 2) {
; #pragma unroll
;                             for (int e = 0; e < 8; ++e) v[e] = sigmoidf_(v[e]);
;                         }
;                         u32x4 w; w.x = pg8::cvt_pk_bf16(v[0], v[1]); w.y = pg8::cvt_pk_bf16(v[2], v[3]); w.z = pg8::cvt_pk_bf16(v[4], v[5]); w.w = pg8::cvt_pk_bf16(v[6], v[7]);
;                         if (NOSTORE) asm volatile("" :: "v"(w)); else st16_stream(base + (size_t)row * D + col, w);
;                     }
.LBB0_233:
	v_lshlrev_b64 v[76:77], 12, v[158:159]
	v_lshl_add_u64 v[76:77], v[76:77], 0, s[44:45]
	v_cvt_pk_bf16_f32 v78, v86, v87
	v_lshl_add_u64 v[82:83], v[134:135], 0, v[76:77]
	v_cvt_pk_bf16_f32 v79, v88, v89
	v_cvt_pk_bf16_f32 v80, v90, v91
	v_cvt_pk_bf16_f32 v81, v94, v95
	global_store_dwordx4 v[82:83], v[78:81], off nt
	s_mov_b64 s[10:11], -1
	s_and_b64 vcc, exec, s[6:7]
	v_or_b32_e32 v78, 0x80, v162
	v_ashrrev_i32_e32 v79, 31, v78
	s_cbranch_vccnz .LBB0_235
	s_cbranch_execnz .LBB0_237
	s_branch .LBB0_236

; DI float sigmoidf_(float x) { return __builtin_amdgcn_rcpf(1.0f + __expf(-x)); }
; DI unsigned cvt_pk_bf16(float lo, float hi) { unsigned r; asm volatile("v_cvt_pk_bf16_f32 %0, %1, %2" : "=v"(r) : "v"(lo), "v"(hi)); return r; }
;     DI void operator()(const f32x4 (&acc)[2][2][4][2], const pg8::Unit& u, int wr, int wc, int fr, int fq) const {
;     ...
; #pragma unroll
;                 for (int ai = 0; ai < 2; ++ai)
; #pragma unroll
;                     for (int m = 0; m < 4; ++m) {
;                         const int row = row0 + ai * 128 + m * 16;
;                         float v[8];
; #pragma unroll
;                         for (int e = 0; e < 4; ++e) { v[e] = acc[ai][bj][m][0][e]; v[4 + e] = acc[ai][bj][m][1][e]; }
;                         if (mode == 1) {
; #pragma unroll
;                             for (int e = 0; e < 8; ++e) v[e] = __logf(lb[e] + (1.0f - lb[e]) * sigmoidf_(v[e]));
;                         } else if (mode == 2) {
; #pragma unroll
;                             for (int e = 0; e < 8; ++e) v[e] = sigmoidf_(v[e]);
;                         }
;                         u32x4 w; w.x = pg8::cvt_pk_bf16(v[0], v[1]); w.y = pg8::cvt_pk_bf16(v[2], v[3]); w.z = pg8::cvt_pk_bf16(v[4], v[5]); w.w = pg8::cvt_pk_bf16(v[6], v[7]);
;                         if (NOSTORE) asm volatile("" :: "v"(w)); else st16_stream(base + (size_t)row * D + col, w);
;                     }
.LBB0_251:
	v_lshl_add_u64 v[68:69], v[78:79], 1, s[56:57]
	v_cvt_pk_bf16_f32 v70, v89, v90
	v_cvt_pk_bf16_f32 v71, v91, v94
	v_cvt_pk_bf16_f32 v72, v95, v96
	v_cvt_pk_bf16_f32 v73, v97, v98
	v_lshl_add_u64 v[74:75], v[68:69], 0, v[132:133]
	s_and_b64 vcc, exec, s[6:7]
	s_mov_b64 s[10:11], -1
	global_store_dwordx4 v[74:75], v[70:73], off nt
	s_cbranch_vccnz .LBB0_254
	s_and_b64 vcc, exec, s[4:5]
	s_cbranch_vccnz .LBB0_289
	v_mul_f32_e32 v70, 0xbfb8aa3b, v64
	v_mul_f32_e32 v71, 0xbfb8aa3b, v65
	v_mul_f32_e32 v72, 0xbfb8aa3b, v66
	v_mul_f32_e32 v73, 0xbfb8aa3b, v67
	v_mul_f32_e32 v74, 0xbfb8aa3b, v60
	v_mul_f32_e32 v75, 0xbfb8aa3b, v61
	v_mul_f32_e32 v78, 0xbfb8aa3b, v62
	v_mul_f32_e32 v79, 0xbfb8aa3b, v63
	v_exp_f32_e32 v70, v70
	v_exp_f32_e32 v71, v71
	v_exp_f32_e32 v72, v72
	v_exp_f32_e32 v73, v73
	v_exp_f32_e32 v74, v74
	v_exp_f32_e32 v75, v75
	v_exp_f32_e32 v78, v78
	v_exp_f32_e32 v79, v79
	v_add_f32_e32 v70, 1.0, v70
	v_add_f32_e32 v71, 1.0, v71
	v_add_f32_e32 v72, 1.0, v72
	v_add_f32_e32 v73, 1.0, v73
	v_add_f32_e32 v74, 1.0, v74
	v_add_f32_e32 v75, 1.0, v75
	v_add_f32_e32 v78, 1.0, v78
	v_add_f32_e32 v79, 1.0, v79
	v_rcp_f32_e32 v70, v70
	v_rcp_f32_e32 v71, v71
	v_rcp_f32_e32 v72, v72
	v_rcp_f32_e32 v73, v73
	v_rcp_f32_e32 v74, v74
	v_rcp_f32_e32 v75, v75
	v_rcp_f32_e32 v78, v78
	v_rcp_f32_e32 v79, v79
	s_mov_b64 s[10:11], 0

; DI float sigmoidf_(float x) { return __builtin_amdgcn_rcpf(1.0f + __expf(-x)); }
; DI unsigned cvt_pk_bf16(float lo, float hi) { unsigned r; asm volatile("v_cvt_pk_bf16_f32 %0, %1, %2" : "=v"(r) : "v"(lo), "v"(hi)); return r; }
;     DI void operator()(const f32x4 (&acc)[2][2][4][2], const pg8::Unit& u, int wr, int wc, int fr, int fq) const {
;     ...
; #pragma unroll
;                 for (int ai = 0; ai < 2; ++ai)
; #pragma unroll
;                     for (int m = 0; m < 4; ++m) {
;                         const int row = row0 + ai * 128 + m * 16;
;                         float v[8];
; #pragma unroll
;                         for (int e = 0; e < 4; ++e) { v[e] = acc[ai][bj][m][0][e]; v[4 + e] = acc[ai][bj][m][1][e]; }
;                         if (mode == 1) {
; #pragma unroll
;                             for (int e = 0; e < 8; ++e) v[e] = __logf(lb[e] + (1.0f - lb[e]) * sigmoidf_(v[e]));
;                         } else if (mode == 2) {
; #pragma unroll
;                             for (int e = 0; e < 8; ++e) v[e] = sigmoidf_(v[e]);
;                         }
;                         u32x4 w; w.x = pg8::cvt_pk_bf16(v[0], v[1]); w.y = pg8::cvt_pk_bf16(v[2], v[3]); w.z = pg8::cvt_pk_bf16(v[4], v[5]); w.w = pg8::cvt_pk_bf16(v[6], v[7]);
;                         if (NOSTORE) asm volatile("" :: "v"(w)); else st16_stream(base + (size_t)row * D + col, w);
;                     }
.LBB0_256:
	v_cvt_pk_bf16_f32 v60, v70, v71
	v_cvt_pk_bf16_f32 v61, v72, v73
	v_cvt_pk_bf16_f32 v62, v74, v75
	v_cvt_pk_bf16_f32 v63, v78, v79
	v_lshl_add_u64 v[64:65], v[68:69], 0, v[124:125]
	s_and_b64 vcc, exec, s[6:7]
	s_mov_b64 s[10:11], -1
	global_store_dwordx4 v[64:65], v[60:63], off nt
	s_cbranch_vccnz .LBB0_259
	s_and_b64 vcc, exec, s[4:5]
	s_cbranch_vccnz .LBB0_290
	v_mul_f32_e32 v60, 0xbfb8aa3b, v56
	v_mul_f32_e32 v61, 0xbfb8aa3b, v57
	v_mul_f32_e32 v62, 0xbfb8aa3b, v58
	v_mul_f32_e32 v63, 0xbfb8aa3b, v59
	v_mul_f32_e32 v64, 0xbfb8aa3b, v52
	v_mul_f32_e32 v65, 0xbfb8aa3b, v53
	v_mul_f32_e32 v66, 0xbfb8aa3b, v54
	v_mul_f32_e32 v67, 0xbfb8aa3b, v55
	v_exp_f32_e32 v60, v60
	v_exp_f32_e32 v61, v61
	v_exp_f32_e32 v62, v62
	v_exp_f32_e32 v63, v63
	v_exp_f32_e32 v64, v64
	v_exp_f32_e32 v65, v65
	v_exp_f32_e32 v66, v66
	v_exp_f32_e32 v67, v67
	v_add_f32_e32 v60, 1.0, v60
	v_add_f32_e32 v61, 1.0, v61
	v_add_f32_e32 v62, 1.0, v62
	v_add_f32_e32 v63, 1.0, v63
	v_add_f32_e32 v64, 1.0, v64
	v_add_f32_e32 v65, 1.0, v65
	v_add_f32_e32 v66, 1.0, v66
	v_add_f32_e32 v67, 1.0, v67
	v_rcp_f32_e32 v60, v60
	v_rcp_f32_e32 v61, v61
	v_rcp_f32_e32 v62, v62
	v_rcp_f32_e32 v63, v63
	v_rcp_f32_e32 v64, v64
	v_rcp_f32_e32 v65, v65
	v_rcp_f32_e32 v66, v66
	v_rcp_f32_e32 v67, v67
	s_mov_b64 s[10:11], 0

; DI float sigmoidf_(float x) { return __builtin_amdgcn_rcpf(1.0f + __expf(-x)); }
; DI unsigned cvt_pk_bf16(float lo, float hi) { unsigned r; asm volatile("v_cvt_pk_bf16_f32 %0, %1, %2" : "=v"(r) : "v"(lo), "v"(hi)); return r; }
;     DI void operator()(const f32x4 (&acc)[2][2][4][2], const pg8::Unit& u, int wr, int wc, int fr, int fq) const {
;     ...
; #pragma unroll
;                 for (int ai = 0; ai < 2; ++ai)
; #pragma unroll
;                     for (int m = 0; m < 4; ++m) {
;                         const int row = row0 + ai * 128 + m * 16;
;                         float v[8];
; #pragma unroll
;                         for (int e = 0; e < 4; ++e) { v[e] = acc[ai][bj][m][0][e]; v[4 + e] = acc[ai][bj][m][1][e]; }
;                         if (mode == 1) {
; #pragma unroll
;                             for (int e = 0; e < 8; ++e) v[e] = __logf(lb[e] + (1.0f - lb[e]) * sigmoidf_(v[e]));
;                         } else if (mode == 2) {
; #pragma unroll
;                             for (int e = 0; e < 8; ++e) v[e] = sigmoidf_(v[e]);
;                         }
;                         u32x4 w; w.x = pg8::cvt_pk_bf16(v[0], v[1]); w.y = pg8::cvt_pk_bf16(v[2], v[3]); w.z = pg8::cvt_pk_bf16(v[4], v[5]); w.w = pg8::cvt_pk_bf16(v[6], v[7]);
;                         if (NOSTORE) asm volatile("" :: "v"(w)); else st16_stream(base + (size_t)row * D + col, w);
;                     }
.LBB0_261:
	v_cvt_pk_bf16_f32 v52, v60, v61
	v_cvt_pk_bf16_f32 v53, v62, v63
	v_cvt_pk_bf16_f32 v54, v64, v65
	v_cvt_pk_bf16_f32 v55, v66, v67
	v_lshl_add_u64 v[56:57], v[68:69], 0, v[116:117]
	s_and_b64 vcc, exec, s[6:7]
	s_mov_b64 s[10:11], -1
	global_store_dwordx4 v[56:57], v[52:55], off nt
	s_cbranch_vccnz .LBB0_264
	s_and_b64 vcc, exec, s[4:5]
	s_cbranch_vccnz .LBB0_291
	v_mul_f32_e32 v52, 0xbfb8aa3b, v48
	v_mul_f32_e32 v53, 0xbfb8aa3b, v49
	v_mul_f32_e32 v54, 0xbfb8aa3b, v50
	v_mul_f32_e32 v55, 0xbfb8aa3b, v51
	v_mul_f32_e32 v56, 0xbfb8aa3b, v44
	v_mul_f32_e32 v57, 0xbfb8aa3b, v45
	v_mul_f32_e32 v58, 0xbfb8aa3b, v46
	v_mul_f32_e32 v59, 0xbfb8aa3b, v47
	v_exp_f32_e32 v52, v52
	v_exp_f32_e32 v53, v53
	v_exp_f32_e32 v54, v54
	v_exp_f32_e32 v55, v55
	v_exp_f32_e32 v56, v56
	v_exp_f32_e32 v57, v57
	v_exp_f32_e32 v58, v58
	v_exp_f32_e32 v59, v59
	v_add_f32_e32 v52, 1.0, v52
	v_add_f32_e32 v53, 1.0, v53
	v_add_f32_e32 v54, 1.0, v54
	v_add_f32_e32 v55, 1.0, v55
	v_add_f32_e32 v56, 1.0, v56
	v_add_f32_e32 v57, 1.0, v57
	v_add_f32_e32 v58, 1.0, v58
	v_add_f32_e32 v59, 1.0, v59
	v_rcp_f32_e32 v52, v52
	v_rcp_f32_e32 v53, v53
	v_rcp_f32_e32 v54, v54
	v_rcp_f32_e32 v55, v55
	v_rcp_f32_e32 v56, v56
	v_rcp_f32_e32 v57, v57
	v_rcp_f32_e32 v58, v58
	v_rcp_f32_e32 v59, v59
	s_mov_b64 s[10:11], 0

; DI float sigmoidf_(float x) { return __builtin_amdgcn_rcpf(1.0f + __expf(-x)); }
; DI unsigned cvt_pk_bf16(float lo, float hi) { unsigned r; asm volatile("v_cvt_pk_bf16_f32 %0, %1, %2" : "=v"(r) : "v"(lo), "v"(hi)); return r; }
;     DI void operator()(const f32x4 (&acc)[2][2][4][2], const pg8::Unit& u, int wr, int wc, int fr, int fq) const {
;     ...
; #pragma unroll
;                 for (int ai = 0; ai < 2; ++ai)
; #pragma unroll
;                     for (int m = 0; m < 4; ++m) {
;                         const int row = row0 + ai * 128 + m * 16;
;                         float v[8];
; #pragma unroll
;                         for (int e = 0; e < 4; ++e) { v[e] = acc[ai][bj][m][0][e]; v[4 + e] = acc[ai][bj][m][1][e]; }
;                         if (mode == 1) {
; #pragma unroll
;                             for (int e = 0; e < 8; ++e) v[e] = __logf(lb[e] + (1.0f - lb[e]) * sigmoidf_(v[e]));
;                         } else if (mode == 2) {
; #pragma unroll
;                             for (int e = 0; e < 8; ++e) v[e] = sigmoidf_(v[e]);
;                         }
;                         u32x4 w; w.x = pg8::cvt_pk_bf16(v[0], v[1]); w.y = pg8::cvt_pk_bf16(v[2], v[3]); w.z = pg8::cvt_pk_bf16(v[4], v[5]); w.w = pg8::cvt_pk_bf16(v[6], v[7]);
;                         if (NOSTORE) asm volatile("" :: "v"(w)); else st16_stream(base + (size_t)row * D + col, w);
;                     }
.LBB0_266:
	v_cvt_pk_bf16_f32 v44, v52, v53
	v_cvt_pk_bf16_f32 v45, v54, v55
	v_cvt_pk_bf16_f32 v46, v56, v57
	v_cvt_pk_bf16_f32 v47, v58, v59
	v_lshl_add_u64 v[48:49], v[68:69], 0, v[108:109]
	s_and_b64 vcc, exec, s[6:7]
	s_mov_b64 s[10:11], -1
	global_store_dwordx4 v[48:49], v[44:47], off nt
	s_cbranch_vccnz .LBB0_269
	s_and_b64 vcc, exec, s[4:5]
	s_cbranch_vccnz .LBB0_292
	v_mul_f32_e32 v44, 0xbfb8aa3b, v40
	v_mul_f32_e32 v45, 0xbfb8aa3b, v41
	v_mul_f32_e32 v46, 0xbfb8aa3b, v42
	v_mul_f32_e32 v47, 0xbfb8aa3b, v43
	v_mul_f32_e32 v48, 0xbfb8aa3b, v36
	v_mul_f32_e32 v49, 0xbfb8aa3b, v37
	v_mul_f32_e32 v50, 0xbfb8aa3b, v38
	v_mul_f32_e32 v51, 0xbfb8aa3b, v39
	v_exp_f32_e32 v44, v44
	v_exp_f32_e32 v45, v45
	v_exp_f32_e32 v46, v46
	v_exp_f32_e32 v47, v47
	v_exp_f32_e32 v48, v48
	v_exp_f32_e32 v49, v49
	v_exp_f32_e32 v50, v50
	v_exp_f32_e32 v51, v51
	v_add_f32_e32 v44, 1.0, v44
	v_add_f32_e32 v45, 1.0, v45
	v_add_f32_e32 v46, 1.0, v46
	v_add_f32_e32 v47, 1.0, v47
	v_add_f32_e32 v48, 1.0, v48
	v_add_f32_e32 v49, 1.0, v49
	v_add_f32_e32 v50, 1.0, v50
	v_add_f32_e32 v51, 1.0, v51
	v_rcp_f32_e32 v44, v44
	v_rcp_f32_e32 v45, v45
	v_rcp_f32_e32 v46, v46
	v_rcp_f32_e32 v47, v47
	v_rcp_f32_e32 v48, v48
	v_rcp_f32_e32 v49, v49
	v_rcp_f32_e32 v50, v50
	v_rcp_f32_e32 v51, v51
	s_mov_b64 s[10:11], 0

; DI float sigmoidf_(float x) { return __builtin_amdgcn_rcpf(1.0f + __expf(-x)); }
; DI unsigned cvt_pk_bf16(float lo, float hi) { unsigned r; asm volatile("v_cvt_pk_bf16_f32 %0, %1, %2" : "=v"(r) : "v"(lo), "v"(hi)); return r; }
;     DI void operator()(const f32x4 (&acc)[2][2][4][2], const pg8::Unit& u, int wr, int wc, int fr, int fq) const {
;     ...
; #pragma unroll
;                 for (int ai = 0; ai < 2; ++ai)
; #pragma unroll
;                     for (int m = 0; m < 4; ++m) {
;                         const int row = row0 + ai * 128 + m * 16;
;                         float v[8];
; #pragma unroll
;                         for (int e = 0; e < 4; ++e) { v[e] = acc[ai][bj][m][0][e]; v[4 + e] = acc[ai][bj][m][1][e]; }
;                         if (mode == 1) {
; #pragma unroll
;                             for (int e = 0; e < 8; ++e) v[e] = __logf(lb[e] + (1.0f - lb[e]) * sigmoidf_(v[e]));
;                         } else if (mode == 2) {
; #pragma unroll
;                             for (int e = 0; e < 8; ++e) v[e] = sigmoidf_(v[e]);
;                         }
;                         u32x4 w; w.x = pg8::cvt_pk_bf16(v[0], v[1]); w.y = pg8::cvt_pk_bf16(v[2], v[3]); w.z = pg8::cvt_pk_bf16(v[4], v[5]); w.w = pg8::cvt_pk_bf16(v[6], v[7]);
;                         if (NOSTORE) asm volatile("" :: "v"(w)); else st16_stream(base + (size_t)row * D + col, w);
;                     }
.LBB0_271:
	v_cvt_pk_bf16_f32 v36, v44, v45
	v_cvt_pk_bf16_f32 v37, v46, v47
	v_cvt_pk_bf16_f32 v38, v48, v49
	v_cvt_pk_bf16_f32 v39, v50, v51
	v_lshl_add_u64 v[40:41], v[68:69], 0, v[100:101]
	s_and_b64 vcc, exec, s[6:7]
	s_mov_b64 s[10:11], -1
	global_store_dwordx4 v[40:41], v[36:39], off nt
	s_cbranch_vccnz .LBB0_274
	s_and_b64 vcc, exec, s[4:5]
	s_cbranch_vccnz .LBB0_293
	v_mul_f32_e32 v36, 0xbfb8aa3b, v32
	v_mul_f32_e32 v37, 0xbfb8aa3b, v33
	v_mul_f32_e32 v38, 0xbfb8aa3b, v34
	v_mul_f32_e32 v39, 0xbfb8aa3b, v35
	v_mul_f32_e32 v40, 0xbfb8aa3b, v28
	v_mul_f32_e32 v41, 0xbfb8aa3b, v29
	v_mul_f32_e32 v42, 0xbfb8aa3b, v30
	v_mul_f32_e32 v43, 0xbfb8aa3b, v31
	v_exp_f32_e32 v36, v36
	v_exp_f32_e32 v37, v37
	v_exp_f32_e32 v38, v38
	v_exp_f32_e32 v39, v39
	v_exp_f32_e32 v40, v40
	v_exp_f32_e32 v41, v41
	v_exp_f32_e32 v42, v42
	v_exp_f32_e32 v43, v43
	v_add_f32_e32 v36, 1.0, v36
	v_add_f32_e32 v37, 1.0, v37
	v_add_f32_e32 v38, 1.0, v38
	v_add_f32_e32 v39, 1.0, v39
	v_add_f32_e32 v40, 1.0, v40
	v_add_f32_e32 v41, 1.0, v41
	v_add_f32_e32 v42, 1.0, v42
	v_add_f32_e32 v43, 1.0, v43
	v_rcp_f32_e32 v36, v36
	v_rcp_f32_e32 v37, v37
	v_rcp_f32_e32 v38, v38
	v_rcp_f32_e32 v39, v39
	v_rcp_f32_e32 v40, v40
	v_rcp_f32_e32 v41, v41
	v_rcp_f32_e32 v42, v42
	v_rcp_f32_e32 v43, v43
	s_mov_b64 s[10:11], 0

; DI float sigmoidf_(float x) { return __builtin_amdgcn_rcpf(1.0f + __expf(-x)); }
; DI unsigned cvt_pk_bf16(float lo, float hi) { unsigned r; asm volatile("v_cvt_pk_bf16_f32 %0, %1, %2" : "=v"(r) : "v"(lo), "v"(hi)); return r; }
;     DI void operator()(const f32x4 (&acc)[2][2][4][2], const pg8::Unit& u, int wr, int wc, int fr, int fq) const {
;     ...
; #pragma unroll
;                 for (int ai = 0; ai < 2; ++ai)
; #pragma unroll
;                     for (int m = 0; m < 4; ++m) {
;                         const int row = row0 + ai * 128 + m * 16;
;                         float v[8];
; #pragma unroll
;                         for (int e = 0; e < 4; ++e) { v[e] = acc[ai][bj][m][0][e]; v[4 + e] = acc[ai][bj][m][1][e]; }
;                         if (mode == 1) {
; #pragma unroll
;                             for (int e = 0; e < 8; ++e) v[e] = __logf(lb[e] + (1.0f - lb[e]) * sigmoidf_(v[e]));
;                         } else if (mode == 2) {
; #pragma unroll
;                             for (int e = 0; e < 8; ++e) v[e] = sigmoidf_(v[e]);
;                         }
;                         u32x4 w; w.x = pg8::cvt_pk_bf16(v[0], v[1]); w.y = pg8::cvt_pk_bf16(v[2], v[3]); w.z = pg8::cvt_pk_bf16(v[4], v[5]); w.w = pg8::cvt_pk_bf16(v[6], v[7]);
;                         if (NOSTORE) asm volatile("" :: "v"(w)); else st16_stream(base + (size_t)row * D + col, w);
;                     }
.LBB0_276:
	v_cvt_pk_bf16_f32 v28, v36, v37
	v_cvt_pk_bf16_f32 v29, v38, v39
	v_cvt_pk_bf16_f32 v30, v40, v41
	v_cvt_pk_bf16_f32 v31, v42, v43
	v_lshl_add_u64 v[32:33], v[68:69], 0, v[92:93]
	s_and_b64 vcc, exec, s[6:7]
	s_mov_b64 s[10:11], -1
	global_store_dwordx4 v[32:33], v[28:31], off nt
	s_cbranch_vccnz .LBB0_279
	s_and_b64 vcc, exec, s[4:5]
	s_cbranch_vccnz .LBB0_294
	v_mul_f32_e32 v28, 0xbfb8aa3b, v24
	v_mul_f32_e32 v29, 0xbfb8aa3b, v25
	v_mul_f32_e32 v30, 0xbfb8aa3b, v26
	v_mul_f32_e32 v31, 0xbfb8aa3b, v27
	v_mul_f32_e32 v32, 0xbfb8aa3b, v20
	v_mul_f32_e32 v33, 0xbfb8aa3b, v21
	v_mul_f32_e32 v34, 0xbfb8aa3b, v22
	v_mul_f32_e32 v35, 0xbfb8aa3b, v23
	v_exp_f32_e32 v28, v28
	v_exp_f32_e32 v29, v29
	v_exp_f32_e32 v30, v30
	v_exp_f32_e32 v31, v31
	v_exp_f32_e32 v32, v32
	v_exp_f32_e32 v33, v33
	v_exp_f32_e32 v34, v34
	v_exp_f32_e32 v35, v35
	v_add_f32_e32 v28, 1.0, v28
	v_add_f32_e32 v29, 1.0, v29
	v_add_f32_e32 v30, 1.0, v30
	v_add_f32_e32 v31, 1.0, v31
	v_add_f32_e32 v32, 1.0, v32
	v_add_f32_e32 v33, 1.0, v33
	v_add_f32_e32 v34, 1.0, v34
	v_add_f32_e32 v35, 1.0, v35
	v_rcp_f32_e32 v28, v28
	v_rcp_f32_e32 v29, v29
	v_rcp_f32_e32 v30, v30
	v_rcp_f32_e32 v31, v31
	v_rcp_f32_e32 v32, v32
	v_rcp_f32_e32 v33, v33
	v_rcp_f32_e32 v34, v34
	v_rcp_f32_e32 v35, v35
	s_mov_b64 s[10:11], 0

; DI float sigmoidf_(float x) { return __builtin_amdgcn_rcpf(1.0f + __expf(-x)); }
; DI unsigned cvt_pk_bf16(float lo, float hi) { unsigned r; asm volatile("v_cvt_pk_bf16_f32 %0, %1, %2" : "=v"(r) : "v"(lo), "v"(hi)); return r; }
;     DI void operator()(const f32x4 (&acc)[2][2][4][2], const pg8::Unit& u, int wr, int wc, int fr, int fq) const {
;     ...
; #pragma unroll
;                 for (int ai = 0; ai < 2; ++ai)
; #pragma unroll
;                     for (int m = 0; m < 4; ++m) {
;                         const int row = row0 + ai * 128 + m * 16;
;                         float v[8];
; #pragma unroll
;                         for (int e = 0; e < 4; ++e) { v[e] = acc[ai][bj][m][0][e]; v[4 + e] = acc[ai][bj][m][1][e]; }
;                         if (mode == 1) {
; #pragma unroll
;                             for (int e = 0; e < 8; ++e) v[e] = __logf(lb[e] + (1.0f - lb[e]) * sigmoidf_(v[e]));
;                         } else if (mode == 2) {
; #pragma unroll
;                             for (int e = 0; e < 8; ++e) v[e] = sigmoidf_(v[e]);
;                         }
;                         u32x4 w; w.x = pg8::cvt_pk_bf16(v[0], v[1]); w.y = pg8::cvt_pk_bf16(v[2], v[3]); w.z = pg8::cvt_pk_bf16(v[4], v[5]); w.w = pg8::cvt_pk_bf16(v[6], v[7]);
;                         if (NOSTORE) asm volatile("" :: "v"(w)); else st16_stream(base + (size_t)row * D + col, w);
;                     }
.LBB0_281:
	v_cvt_pk_bf16_f32 v20, v28, v29
	v_cvt_pk_bf16_f32 v21, v30, v31
	v_cvt_pk_bf16_f32 v22, v32, v33
	v_cvt_pk_bf16_f32 v23, v34, v35
	v_lshl_add_u64 v[24:25], v[68:69], 0, v[84:85]
	s_and_b64 vcc, exec, s[6:7]
	s_mov_b64 s[6:7], -1
	global_store_dwordx4 v[24:25], v[20:23], off nt
	s_cbranch_vccnz .LBB0_284
	s_and_b64 vcc, exec, s[4:5]
	s_cbranch_vccnz .LBB0_295
	v_mul_f32_e32 v20, 0xbfb8aa3b, v16
	v_mul_f32_e32 v21, 0xbfb8aa3b, v17
	v_mul_f32_e32 v22, 0xbfb8aa3b, v18
	v_mul_f32_e32 v23, 0xbfb8aa3b, v19
	v_mul_f32_e32 v24, 0xbfb8aa3b, v12
	v_mul_f32_e32 v25, 0xbfb8aa3b, v13
	v_mul_f32_e32 v26, 0xbfb8aa3b, v14
	v_mul_f32_e32 v27, 0xbfb8aa3b, v15
	v_exp_f32_e32 v20, v20
	v_exp_f32_e32 v21, v21
	v_exp_f32_e32 v22, v22
	v_exp_f32_e32 v23, v23
	v_exp_f32_e32 v24, v24
	v_exp_f32_e32 v25, v25
	v_exp_f32_e32 v26, v26
	v_exp_f32_e32 v27, v27
	v_add_f32_e32 v20, 1.0, v20
	v_add_f32_e32 v21, 1.0, v21
	v_add_f32_e32 v22, 1.0, v22
	v_add_f32_e32 v23, 1.0, v23
	v_add_f32_e32 v24, 1.0, v24
	v_add_f32_e32 v25, 1.0, v25
	v_add_f32_e32 v26, 1.0, v26
	v_add_f32_e32 v27, 1.0, v27
	v_rcp_f32_e32 v20, v20
	v_rcp_f32_e32 v21, v21
	v_rcp_f32_e32 v22, v22
	v_rcp_f32_e32 v23, v23
	v_rcp_f32_e32 v24, v24
	v_rcp_f32_e32 v25, v25
	v_rcp_f32_e32 v26, v26
	v_rcp_f32_e32 v27, v27
	s_mov_b64 s[6:7], 0

; DI float sigmoidf_(float x) { return __builtin_amdgcn_rcpf(1.0f + __expf(-x)); }
; DI unsigned cvt_pk_bf16(float lo, float hi) { unsigned r; asm volatile("v_cvt_pk_bf16_f32 %0, %1, %2" : "=v"(r) : "v"(lo), "v"(hi)); return r; }
;     DI void operator()(const f32x4 (&acc)[2][2][4][2], const pg8::Unit& u, int wr, int wc, int fr, int fq) const {
;     ...
; #pragma unroll
;                 for (int ai = 0; ai < 2; ++ai)
; #pragma unroll
;                     for (int m = 0; m < 4; ++m) {
;                         const int row = row0 + ai * 128 + m * 16;
;                         float v[8];
; #pragma unroll
;                         for (int e = 0; e < 4; ++e) { v[e] = acc[ai][bj][m][0][e]; v[4 + e] = acc[ai][bj][m][1][e]; }
;                         if (mode == 1) {
; #pragma unroll
;                             for (int e = 0; e < 8; ++e) v[e] = __logf(lb[e] + (1.0f - lb[e]) * sigmoidf_(v[e]));
;                         } else if (mode == 2) {
; #pragma unroll
;                             for (int e = 0; e < 8; ++e) v[e] = sigmoidf_(v[e]);
;                         }
;                         u32x4 w; w.x = pg8::cvt_pk_bf16(v[0], v[1]); w.y = pg8::cvt_pk_bf16(v[2], v[3]); w.z = pg8::cvt_pk_bf16(v[4], v[5]); w.w = pg8::cvt_pk_bf16(v[6], v[7]);
;                         if (NOSTORE) asm volatile("" :: "v"(w)); else st16_stream(base + (size_t)row * D + col, w);
;                     }
.LBB0_286:
	v_lshl_add_u64 v[8:9], v[68:69], 0, v[76:77]
	v_cvt_pk_bf16_f32 v4, v20, v21
	v_cvt_pk_bf16_f32 v5, v22, v23
	v_cvt_pk_bf16_f32 v6, v24, v25
	v_cvt_pk_bf16_f32 v7, v26, v27
	global_store_dwordx4 v[8:9], v[4:7], off nt
	s_andn2_b64 vcc, exec, s[8:9]
	s_mov_b64 s[4:5], -1
	s_cbranch_vccnz .LBB0_99
